# attention-A: conversion pads filled with first max ops; P4 epilogue: removed no-op canonicalising v_max on converted gate values
# speedup vs baseline: 1.0772x; 1.0007x over previous
.LBB0_419:
	v_mfma_scale_f32_32x32x64_f8f6f4 v[112:127], v[228:233], v[182:187], v[80:95], v217, v216 op_sel_hi:[0,0,0] cbsz:2 blgp:2
	v_exp_f32_e32 v128, v128
	v_exp_f32_e32 v129, v129
	v_exp_f32_e32 v130, v130
	v_exp_f32_e32 v131, v131
	v_mfma_scale_f32_32x32x64_f8f6f4 v[96:111], v[234:239], v[182:187], v[80:95], v217, v216 op_sel_hi:[0,0,0] cbsz:2 blgp:2
	v_exp_f32_e32 v132, v132
	v_exp_f32_e32 v133, v133
	v_exp_f32_e32 v134, v134
	v_exp_f32_e32 v135, v135
	v_mfma_scale_f32_32x32x64_f8f6f4 v[112:127], v[240:245], v[176:181], v[112:127], v217, v216 op_sel_hi:[0,0,0] cbsz:2 blgp:2
	v_exp_f32_e32 v136, v136
	v_exp_f32_e32 v137, v137
	v_exp_f32_e32 v138, v138
	v_exp_f32_e32 v139, v139
	v_mfma_scale_f32_32x32x64_f8f6f4 v[96:111], v[246:251], v[176:181], v[96:111], v217, v216 op_sel_hi:[0,0,0] cbsz:2 blgp:2
	ds_read_b128 v[228:231], v223
	ds_read_b64 v[232:233], v224
	ds_read_b128 v[234:237], v223 offset:4096
	ds_read_b64 v[238:239], v224 offset:4096
	ds_read_b128 v[240:243], v221
	ds_read_b64 v[244:245], v222
	ds_read_b128 v[246:249], v221 offset:4096
	ds_read_b64 v[250:251], v222 offset:4096
	ds_read_b128 v[206:209], v163 offset:24576
	ds_read_b64 v[210:211], v220 offset:24576
	ds_read_b128 v[200:203], v163 offset:26624
	ds_read_b64 v[204:205], v220 offset:26624
	ds_read_b128 v[194:197], v163 offset:28672
	ds_read_b64 v[198:199], v220 offset:28672
	ds_read_b128 v[188:191], v163 offset:30720
	ds_read_b64 v[192:193], v220 offset:30720
	v_exp_f32_e32 v140, v140
	v_exp_f32_e32 v141, v141
	v_exp_f32_e32 v142, v142
	v_exp_f32_e32 v143, v143
	v_max_f32_e32 v225, v113, v113
	v_cvt_scalef32_2xpk16_bf6_f32 v[128:133], v[144:159], v[128:143], 1.0
	v_max_f32_e32 v226, v112, v112
	v_max_f32_e32 v225, v226, v225
	v_mfma_scale_f32_32x32x64_f8f6f4 v[64:79], v[128:133], v[168:173], v[64:79], v218, v218 op_sel_hi:[0,0,0] cbsz:3 blgp:2
	v_max3_f32 v225, v225, v114, v115
	s_waitcnt lgkmcnt(0)
	v_mfma_scale_f32_32x32x64_f8f6f4 v[0:15], v[128:133], v[206:211], v[0:15], v218, v217 op_sel_hi:[0,0,0] cbsz:3 blgp:2
	v_max3_f32 v225, v225, v116, v117
	v_max3_f32 v225, v225, v118, v119
	v_max3_f32 v225, v225, v120, v121
	v_max3_f32 v225, v225, v122, v123
	v_mfma_scale_f32_32x32x64_f8f6f4 v[48:63], v[128:133], v[200:205], v[48:63], v218, v217 op_sel_hi:[0,0,0] cbsz:3 blgp:2
	v_max3_f32 v225, v225, v124, v125
	v_max3_f32 v225, v225, v126, v127
	v_max3_f32 v225, v225, v96, v97
	v_max3_f32 v225, v225, v98, v99
	v_mfma_scale_f32_32x32x64_f8f6f4 v[32:47], v[128:133], v[194:199], v[32:47], v218, v217 op_sel_hi:[0,0,0] cbsz:3 blgp:2
	v_max3_f32 v225, v225, v100, v101
	v_max3_f32 v225, v225, v102, v103
	v_max3_f32 v225, v225, v104, v105
	v_max3_f32 v225, v225, v106, v107
	v_mfma_scale_f32_32x32x64_f8f6f4 v[16:31], v[128:133], v[188:193], v[16:31], v218, v217 op_sel_hi:[0,0,0] cbsz:3 blgp:2
	v_max3_f32 v225, v225, v108, v109
	v_max3_f32 v225, v225, v110, v111
	v_cmp_nge_f32_e32 vcc, s2, v225
	s_cbranch_vccnz .LBB0_444

.LBB0_437:
	v_mfma_scale_f32_32x32x64_f8f6f4 v[144:159], v[228:233], v[182:187], v[80:95], v217, v216 op_sel_hi:[0,0,0] cbsz:2 blgp:2
	v_exp_f32_e32 v96, v96
	v_exp_f32_e32 v97, v97
	v_exp_f32_e32 v98, v98
	v_exp_f32_e32 v99, v99
	v_mfma_scale_f32_32x32x64_f8f6f4 v[128:143], v[234:239], v[182:187], v[80:95], v217, v216 op_sel_hi:[0,0,0] cbsz:2 blgp:2
	v_exp_f32_e32 v100, v100
	v_exp_f32_e32 v101, v101
	v_exp_f32_e32 v102, v102
	v_exp_f32_e32 v103, v103
	v_mfma_scale_f32_32x32x64_f8f6f4 v[144:159], v[240:245], v[176:181], v[144:159], v217, v216 op_sel_hi:[0,0,0] cbsz:2 blgp:2
	v_exp_f32_e32 v104, v104
	v_exp_f32_e32 v105, v105
	v_exp_f32_e32 v106, v106
	v_exp_f32_e32 v107, v107
	v_mfma_scale_f32_32x32x64_f8f6f4 v[128:143], v[246:251], v[176:181], v[128:143], v217, v216 op_sel_hi:[0,0,0] cbsz:2 blgp:2
	ds_read_b128 v[228:231], v223 offset:8192
	ds_read_b64 v[232:233], v224 offset:8192
	ds_read_b128 v[234:237], v223 offset:12288
	ds_read_b64 v[238:239], v224 offset:12288
	ds_read_b128 v[240:243], v221 offset:8192
	ds_read_b64 v[244:245], v222 offset:8192
	ds_read_b128 v[246:249], v221 offset:12288
	ds_read_b64 v[250:251], v222 offset:12288
	ds_read_b128 v[206:209], v163 offset:32768
	ds_read_b64 v[210:211], v220 offset:32768
	ds_read_b128 v[200:203], v163 offset:34816
	ds_read_b64 v[204:205], v220 offset:34816
	ds_read_b128 v[194:197], v163 offset:36864
	ds_read_b64 v[198:199], v220 offset:36864
	ds_read_b128 v[188:191], v163 offset:38912
	ds_read_b64 v[192:193], v220 offset:38912
	v_exp_f32_e32 v108, v108
	v_exp_f32_e32 v109, v109
	v_exp_f32_e32 v110, v110
	v_exp_f32_e32 v111, v111
	v_max_f32_e32 v212, v145, v145
	v_cvt_scalef32_2xpk16_bf6_f32 v[96:101], v[112:127], v[96:111], 1.0
	v_max_f32_e32 v213, v144, v144
	v_max_f32_e32 v212, v213, v212
	v_mfma_scale_f32_32x32x64_f8f6f4 v[64:79], v[96:101], v[168:173], v[64:79], v218, v218 op_sel_hi:[0,0,0] cbsz:3 blgp:2
	v_max3_f32 v212, v212, v146, v147
	s_waitcnt lgkmcnt(0)
	v_mfma_scale_f32_32x32x64_f8f6f4 v[0:15], v[96:101], v[206:211], v[0:15], v218, v217 op_sel_hi:[0,0,0] cbsz:3 blgp:2
	v_max3_f32 v212, v212, v148, v149
	v_max3_f32 v212, v212, v150, v151
	v_max3_f32 v212, v212, v152, v153
	v_max3_f32 v212, v212, v154, v155
	v_mfma_scale_f32_32x32x64_f8f6f4 v[48:63], v[96:101], v[200:205], v[48:63], v218, v217 op_sel_hi:[0,0,0] cbsz:3 blgp:2
	v_max3_f32 v212, v212, v156, v157
	v_max3_f32 v212, v212, v158, v159
	v_max3_f32 v212, v212, v128, v129
	v_max3_f32 v212, v212, v130, v131
	v_mfma_scale_f32_32x32x64_f8f6f4 v[32:47], v[96:101], v[194:199], v[32:47], v218, v217 op_sel_hi:[0,0,0] cbsz:3 blgp:2
	v_max3_f32 v212, v212, v132, v133
	v_max3_f32 v212, v212, v134, v135
	v_max3_f32 v212, v212, v136, v137
	v_max3_f32 v212, v212, v138, v139
	v_mfma_scale_f32_32x32x64_f8f6f4 v[16:31], v[96:101], v[188:193], v[16:31], v218, v217 op_sel_hi:[0,0,0] cbsz:3 blgp:2
	v_max3_f32 v212, v212, v140, v141
	v_max3_f32 v212, v212, v142, v143
	v_cmp_nge_f32_e32 vcc, s2, v212
	s_cbranch_vccnz .LBB0_445

.LBB0_817:
	v_mov_b32_e32 v16, v200
	global_load_dwordx4 v[8:11], v16, s[16:17] offset:2048
	global_load_dwordx4 v[2:5], v16, s[16:17]
	s_andn2_b64 vcc, exec, s[12:13]
	s_waitcnt vmcnt(0)
	v_cvt_f32_fp8_sdwa v6, v8 src0_sel:BYTE_1
	v_cvt_f32_fp8_e32 v1, v2
	v_cvt_f32_fp8_sdwa v7, v2 src0_sel:BYTE_1
	v_cvt_f32_fp8_sdwa v12, v8 src0_sel:BYTE_2
	v_cvt_f32_fp8_sdwa v13, v2 src0_sel:BYTE_2
	v_cvt_f32_fp8_sdwa v2, v2 src0_sel:BYTE_3
	v_cvt_f32_fp8_e32 v0, v8
	v_cvt_f32_fp8_sdwa v8, v8 src0_sel:BYTE_3
	v_cvt_f32_fp8_e32 v14, v9
	v_cvt_f32_fp8_sdwa v17, v9 src0_sel:BYTE_1
	v_cvt_f32_fp8_sdwa v19, v9 src0_sel:BYTE_2
	v_cvt_f32_fp8_e32 v15, v3
	v_cvt_f32_fp8_sdwa v18, v3 src0_sel:BYTE_1
	v_cvt_f32_fp8_sdwa v20, v3 src0_sel:BYTE_2
	v_cvt_f32_fp8_sdwa v3, v3 src0_sel:BYTE_3
	v_mul_f32_e32 v1, 0xbfb8aa3b, v1
	v_mul_f32_e32 v7, 0xbfb8aa3b, v7
	v_max_f32_e32 v6, v6, v6
	v_max_f32_e32 v12, v12, v12
	v_mul_f32_e32 v13, 0xbfb8aa3b, v13
	v_mul_f32_e32 v2, 0xbfb8aa3b, v2
	v_exp_f32_e32 v21, v1
	v_exp_f32_e32 v24, v7
	v_max_f32_e32 v0, v0, v0
	v_max_f32_e32 v8, v8, v8
	v_max_f32_e32 v14, v14, v14
	v_max_f32_e32 v17, v17, v17
	v_max_f32_e32 v19, v19, v19
	v_max_f32_e32 v1, 0xc1f00000, v6
	v_max_f32_e32 v6, 0xc1f00000, v12
	v_exp_f32_e32 v12, v13
	v_exp_f32_e32 v13, v2
	v_cvt_f32_fp8_sdwa v9, v9 src0_sel:BYTE_3
	v_mul_f32_e32 v3, 0xbfb8aa3b, v3
	v_max_f32_e32 v0, 0xc1f00000, v0
	v_max_f32_e32 v7, 0xc1f00000, v8
	v_max_f32_e32 v2, 0xc1f00000, v14
	v_max_f32_e32 v8, 0xc1f00000, v17
	v_max_f32_e32 v17, 0xc1f00000, v19
	v_mul_f32_e32 v15, 0xbfb8aa3b, v15
	v_mul_f32_e32 v18, 0xbfb8aa3b, v18
	v_mul_f32_e32 v20, 0xbfb8aa3b, v20
	v_exp_f32_e32 v19, v3
	v_mul_f32_e32 v0, 0xbfb8aa3b, v0
	v_mul_f32_e32 v1, 0xbfb8aa3b, v1
	v_mul_f32_e32 v3, 0xbfb8aa3b, v6
	v_mul_f32_e32 v6, 0xbfb8aa3b, v7
	v_mul_f32_e32 v7, 0xbfb8aa3b, v2
	v_mul_f32_e32 v8, 0xbfb8aa3b, v8
	v_mul_f32_e32 v17, 0xbfb8aa3b, v17
	v_exp_f32_e32 v14, v15
	v_exp_f32_e32 v15, v18
	v_exp_f32_e32 v18, v20
	v_exp_f32_e32 v0, v0
	v_exp_f32_e32 v1, v1
	v_exp_f32_e32 v2, v3
	v_exp_f32_e32 v3, v6
	v_exp_f32_e32 v6, v7
	v_exp_f32_e32 v7, v8
	v_exp_f32_e32 v8, v17
	v_add_f32_e32 v17, 1.0, v21
	v_add_f32_e32 v20, 1.0, v24
	v_add_f32_e32 v21, 1.0, v12
	v_add_f32_e32 v24, 1.0, v13
	v_rcp_f32_e32 v12, v17
	v_rcp_f32_e32 v13, v20
	v_cvt_f32_fp8_e32 v23, v4
	v_max_f32_e32 v9, v9, v9
	v_max_f32_e32 v9, 0xc1f00000, v9
	v_cvt_f32_fp8_e32 v22, v10
	v_mul_f32_e32 v9, 0xbfb8aa3b, v9
	v_add_f32_e32 v25, 1.0, v14
	v_add_f32_e32 v26, 1.0, v15
	v_pk_add_f32 v[0:1], v[0:1], 1.0 op_sel_hi:[1,0]
	v_exp_f32_e32 v9, v9
	v_add_f32_e32 v27, 1.0, v18
	v_add_f32_e32 v28, 1.0, v19
	v_rcp_f32_e32 v18, v25
	v_rcp_f32_e32 v19, v26
	v_pk_mul_f32 v[0:1], v[0:1], v[12:13]
	v_rcp_f32_e32 v14, v21
	v_rcp_f32_e32 v15, v24
	v_rcp_f32_e32 v20, v27
	v_rcp_f32_e32 v21, v28
	v_pk_mul_f32 v[158:159], v[158:159], v[0:1]
	v_mul_f32_e32 v1, 0xbfb8aa3b, v23
	v_exp_f32_e32 v1, v1
	v_pk_add_f32 v[6:7], v[6:7], 1.0 op_sel_hi:[1,0]
	v_max_f32_e32 v0, v22, v22
	v_pk_add_f32 v[2:3], v[2:3], 1.0 op_sel_hi:[1,0]
	v_pk_add_f32 v[8:9], v[8:9], 1.0 op_sel_hi:[1,0]
	v_pk_mul_f32 v[6:7], v[6:7], v[18:19]
	v_max_f32_e32 v0, 0xc1f00000, v0
	v_pk_mul_f32 v[2:3], v[2:3], v[14:15]
	v_pk_mul_f32 v[8:9], v[8:9], v[20:21]
	v_pk_mul_f32 v[154:155], v[154:155], v[6:7]
	v_mul_f32_e32 v0, 0xbfb8aa3b, v0
	v_add_u32_e32 v6, 0x10000, v16
	v_pk_mul_f32 v[160:161], v[160:161], v[2:3]
	v_pk_mul_f32 v[156:157], v[156:157], v[8:9]
	v_exp_f32_e32 v12, v0
	v_add_f32_e32 v13, 1.0, v1
	global_load_dwordx4 v[0:3], v6, s[16:17]
	s_nop 0
	global_load_dwordx4 v[6:9], v6, s[16:17] offset:2048
	v_cvt_f32_fp8_sdwa v15, v10 src0_sel:BYTE_1
	v_cvt_f32_fp8_sdwa v17, v4 src0_sel:BYTE_1
	v_cvt_f32_fp8_sdwa v18, v4 src0_sel:BYTE_2
	v_rcp_f32_e32 v14, v13
	v_max_f32_e32 v13, v15, v15
	v_mul_f32_e32 v15, 0xbfb8aa3b, v17
	v_cvt_f32_fp8_sdwa v17, v10 src0_sel:BYTE_2
	v_cvt_f32_fp8_sdwa v10, v10 src0_sel:BYTE_3
	v_cvt_f32_fp8_sdwa v4, v4 src0_sel:BYTE_3
	v_mul_f32_e32 v18, 0xbfb8aa3b, v18
	v_exp_f32_e32 v15, v15
	v_exp_f32_e32 v19, v18
	v_max_f32_e32 v17, v17, v17
	v_max_f32_e32 v13, 0xc1f00000, v13
	v_max_f32_e32 v17, 0xc1f00000, v17
	v_max_f32_e32 v10, 0xc1f00000, v10
	v_mul_f32_e32 v4, 0xbfb8aa3b, v4
	v_mul_f32_e32 v13, 0xbfb8aa3b, v13
	v_mul_f32_e32 v17, 0xbfb8aa3b, v17
	v_exp_f32_e32 v4, v4
	v_mul_f32_e32 v10, 0xbfb8aa3b, v10
	v_exp_f32_e32 v13, v13
	v_add_f32_e32 v15, 1.0, v15
	v_exp_f32_e32 v18, v17
	v_add_f32_e32 v17, 1.0, v19
	v_exp_f32_e32 v19, v10
	v_cvt_f32_fp8_e32 v10, v5
	v_rcp_f32_e32 v15, v15
	v_add_f32_e32 v4, 1.0, v4
	v_rcp_f32_e32 v21, v4
	v_pk_add_f32 v[12:13], v[12:13], 1.0 op_sel_hi:[1,0]
	v_cvt_f32_fp8_e32 v4, v11
	v_mul_f32_e32 v10, 0xbfb8aa3b, v10
	v_rcp_f32_e32 v20, v17
	v_pk_mul_f32 v[12:13], v[12:13], v[14:15]
	v_exp_f32_e32 v10, v10
	v_pk_mul_f32 v[150:151], v[150:151], v[12:13]
	v_cvt_f32_fp8_sdwa v13, v5 src0_sel:BYTE_1
	v_pk_add_f32 v[18:19], v[18:19], 1.0 op_sel_hi:[1,0]
	v_pk_mul_f32 v[14:15], v[18:19], v[20:21]
	v_max_f32_e32 v4, 0xc1f00000, v4
	v_add_f32_e32 v10, 1.0, v10
	v_pk_mul_f32 v[152:153], v[152:153], v[14:15]
	v_mul_f32_e32 v4, 0xbfb8aa3b, v4
	v_rcp_f32_e32 v14, v10
	v_mul_f32_e32 v10, 0xbfb8aa3b, v13
	v_exp_f32_e32 v12, v4
	v_cvt_f32_fp8_sdwa v4, v11 src0_sel:BYTE_1
	v_exp_f32_e32 v10, v10
	v_max_f32_e32 v4, v4, v4
	v_add_f32_e32 v10, 1.0, v10
	v_max_f32_e32 v4, 0xc1f00000, v4
	v_rcp_f32_e32 v15, v10
	v_cvt_f32_fp8_sdwa v10, v5 src0_sel:BYTE_2
	v_cvt_f32_fp8_sdwa v5, v5 src0_sel:BYTE_3
	v_mul_f32_e32 v4, 0xbfb8aa3b, v4
	v_exp_f32_e32 v13, v4
	v_cvt_f32_fp8_sdwa v4, v11 src0_sel:BYTE_2
	v_cvt_f32_fp8_sdwa v11, v11 src0_sel:BYTE_3
	v_mul_f32_e32 v10, 0xbfb8aa3b, v10
	v_mul_f32_e32 v5, 0xbfb8aa3b, v5
	v_exp_f32_e32 v10, v10
	v_exp_f32_e32 v17, v5
	v_max_f32_e32 v4, v4, v4
	v_max_f32_e32 v4, 0xc1f00000, v4
	v_max_f32_e32 v11, 0xc1f00000, v11
	v_mul_f32_e32 v4, 0xbfb8aa3b, v4
	v_mul_f32_e32 v5, 0xbfb8aa3b, v11
	v_exp_f32_e32 v4, v4
	v_add_f32_e32 v10, 1.0, v10
	v_exp_f32_e32 v5, v5
	v_add_f32_e32 v11, 1.0, v17
	v_rcp_f32_e32 v10, v10
	v_rcp_f32_e32 v11, v11
	v_pk_add_f32 v[4:5], v[4:5], 1.0 op_sel_hi:[1,0]
	v_pk_add_f32 v[12:13], v[12:13], 1.0 op_sel_hi:[1,0]
	s_waitcnt vmcnt(0)
	v_cvt_f32_fp8_sdwa v17, v2 src0_sel:BYTE_1
	v_pk_mul_f32 v[4:5], v[4:5], v[10:11]
	v_cvt_f32_fp8_e32 v10, v6
	v_pk_mul_f32 v[148:149], v[148:149], v[4:5]
	v_cvt_f32_fp8_e32 v4, v0
	v_cvt_f32_fp8_sdwa v11, v0 src0_sel:BYTE_1
	v_max_f32_e32 v5, v10, v10
	v_pk_mul_f32 v[12:13], v[12:13], v[14:15]
	v_max_f32_e32 v5, 0xc1f00000, v5
	v_mul_f32_e32 v4, 0xbfb8aa3b, v4
	v_pk_mul_f32 v[146:147], v[146:147], v[12:13]
	v_exp_f32_e32 v10, v4
	v_mul_f32_e32 v4, 0xbfb8aa3b, v5
	v_cvt_f32_fp8_sdwa v5, v6 src0_sel:BYTE_1
	v_cvt_f32_fp8_sdwa v13, v0 src0_sel:BYTE_2
	v_mul_f32_e32 v11, 0xbfb8aa3b, v11
	v_cvt_f32_fp8_sdwa v12, v6 src0_sel:BYTE_2
	v_cvt_f32_fp8_sdwa v6, v6 src0_sel:BYTE_3
	v_exp_f32_e32 v11, v11
	v_cvt_f32_fp8_sdwa v0, v0 src0_sel:BYTE_3
	v_mul_f32_e32 v13, 0xbfb8aa3b, v13
	v_max_f32_e32 v5, 0xc1f00000, v5
	v_exp_f32_e32 v13, v13
	v_mul_f32_e32 v5, 0xbfb8aa3b, v5
	v_exp_f32_e32 v4, v4
	v_add_f32_e32 v10, 1.0, v10
	v_exp_f32_e32 v5, v5
	v_add_f32_e32 v11, 1.0, v11
	v_max_f32_e32 v6, 0xc1f00000, v6
	v_mul_f32_e32 v0, 0xbfb8aa3b, v0
	v_rcp_f32_e32 v10, v10
	v_rcp_f32_e32 v11, v11
	v_exp_f32_e32 v0, v0
	v_mul_f32_e32 v6, 0xbfb8aa3b, v6
	v_add_f32_e32 v14, 1.0, v13
	v_exp_f32_e32 v13, v6
	v_cvt_f32_fp8_e32 v6, v1
	v_max_f32_e32 v12, v12, v12
	v_max_f32_e32 v12, 0xc1f00000, v12
	v_pk_add_f32 v[4:5], v[4:5], 1.0 op_sel_hi:[1,0]
	v_mul_f32_e32 v12, 0xbfb8aa3b, v12
	v_add_f32_e32 v0, 1.0, v0
	v_pk_mul_f32 v[4:5], v[4:5], v[10:11]
	v_exp_f32_e32 v12, v12
	v_rcp_f32_e32 v15, v0
	v_cvt_f32_fp8_e32 v0, v7
	v_pk_mul_f32 v[142:143], v[142:143], v[4:5]
	v_mul_f32_e32 v4, 0xbfb8aa3b, v6
	v_rcp_f32_e32 v14, v14
	v_exp_f32_e32 v5, v4
	v_cvt_f32_fp8_sdwa v6, v1 src0_sel:BYTE_1
	v_pk_add_f32 v[12:13], v[12:13], 1.0 op_sel_hi:[1,0]
	v_pk_mul_f32 v[10:11], v[12:13], v[14:15]
	v_max_f32_e32 v0, 0xc1f00000, v0
	v_add_f32_e32 v5, 1.0, v5
	v_pk_mul_f32 v[144:145], v[144:145], v[10:11]
	v_mul_f32_e32 v0, 0xbfb8aa3b, v0
	v_rcp_f32_e32 v10, v5
	v_mul_f32_e32 v5, 0xbfb8aa3b, v6
	v_exp_f32_e32 v4, v0
	v_cvt_f32_fp8_sdwa v0, v7 src0_sel:BYTE_1
	v_exp_f32_e32 v6, v5
	v_cvt_f32_fp8_sdwa v15, v8 src0_sel:BYTE_1
	v_cvt_f32_fp8_sdwa v18, v2 src0_sel:BYTE_2
	v_add_f32_e32 v6, 1.0, v6
	v_max_f32_e32 v0, 0xc1f00000, v0
	v_rcp_f32_e32 v11, v6
	v_cvt_f32_fp8_sdwa v6, v1 src0_sel:BYTE_2
	v_cvt_f32_fp8_sdwa v1, v1 src0_sel:BYTE_3
	v_mul_f32_e32 v0, 0xbfb8aa3b, v0
	v_exp_f32_e32 v5, v0
	v_cvt_f32_fp8_sdwa v0, v7 src0_sel:BYTE_2
	v_cvt_f32_fp8_sdwa v7, v7 src0_sel:BYTE_3
	v_mul_f32_e32 v6, 0xbfb8aa3b, v6
	v_mul_f32_e32 v1, 0xbfb8aa3b, v1
	v_exp_f32_e32 v6, v6
	v_exp_f32_e32 v12, v1
	v_max_f32_e32 v0, v0, v0
	v_max_f32_e32 v0, 0xc1f00000, v0
	v_max_f32_e32 v7, 0xc1f00000, v7
	v_mul_f32_e32 v0, 0xbfb8aa3b, v0
	v_mul_f32_e32 v1, 0xbfb8aa3b, v7
	v_exp_f32_e32 v0, v0
	v_add_f32_e32 v6, 1.0, v6
	v_exp_f32_e32 v1, v1
	v_add_f32_e32 v7, 1.0, v12
	v_rcp_f32_e32 v6, v6
	v_rcp_f32_e32 v7, v7
	v_pk_add_f32 v[0:1], v[0:1], 1.0 op_sel_hi:[1,0]
	v_pk_add_f32 v[4:5], v[4:5], 1.0 op_sel_hi:[1,0]
	v_mul_f32_e32 v18, 0xbfb8aa3b, v18
	v_pk_mul_f32 v[0:1], v[0:1], v[6:7]
	v_cvt_f32_fp8_e32 v6, v8
	v_cvt_f32_fp8_e32 v7, v2
	v_pk_mul_f32 v[4:5], v[4:5], v[10:11]
	v_add_u32_e32 v10, 0x20000, v16
	v_pk_mul_f32 v[140:141], v[140:141], v[0:1]
	v_pk_mul_f32 v[138:139], v[138:139], v[4:5]
	v_max_f32_e32 v0, v6, v6
	v_mul_f32_e32 v1, 0xbfb8aa3b, v7
	global_load_dwordx4 v[4:7], v10, s[16:17]
	s_nop 0
	global_load_dwordx4 v[10:13], v10, s[16:17] offset:2048
	v_exp_f32_e32 v1, v1
	v_cvt_f32_fp8_sdwa v2, v2 src0_sel:BYTE_3
	v_max_f32_e32 v0, 0xc1f00000, v0
	v_exp_f32_e32 v19, v18
	v_add_f32_e32 v1, 1.0, v1
	v_rcp_f32_e32 v14, v1
	v_max_f32_e32 v1, v15, v15
	v_mul_f32_e32 v15, 0xbfb8aa3b, v17
	v_cvt_f32_fp8_sdwa v17, v8 src0_sel:BYTE_2
	v_cvt_f32_fp8_sdwa v8, v8 src0_sel:BYTE_3
	v_exp_f32_e32 v15, v15
	v_max_f32_e32 v1, 0xc1f00000, v1
	v_mul_f32_e32 v2, 0xbfb8aa3b, v2
	v_mul_f32_e32 v0, 0xbfb8aa3b, v0
	v_mul_f32_e32 v1, 0xbfb8aa3b, v1
	v_exp_f32_e32 v2, v2
	v_exp_f32_e32 v0, v0
	v_exp_f32_e32 v1, v1
	v_add_f32_e32 v15, 1.0, v15
	v_max_f32_e32 v17, 0xc1f00000, v17
	v_max_f32_e32 v8, 0xc1f00000, v8
	v_rcp_f32_e32 v15, v15
	v_mul_f32_e32 v17, 0xbfb8aa3b, v17
	v_mul_f32_e32 v8, 0xbfb8aa3b, v8
	v_exp_f32_e32 v18, v17
	v_add_f32_e32 v17, 1.0, v19
	v_exp_f32_e32 v19, v8
	v_cvt_f32_fp8_e32 v8, v3
	v_add_f32_e32 v2, 1.0, v2
	v_rcp_f32_e32 v21, v2
	v_pk_add_f32 v[0:1], v[0:1], 1.0 op_sel_hi:[1,0]
	v_cvt_f32_fp8_e32 v2, v9
	v_pk_mul_f32 v[0:1], v[0:1], v[14:15]
	v_rcp_f32_e32 v20, v17
	v_pk_mul_f32 v[134:135], v[134:135], v[0:1]
	v_mul_f32_e32 v1, 0xbfb8aa3b, v8
	v_exp_f32_e32 v1, v1
	v_max_f32_e32 v0, v2, v2
	v_cvt_f32_fp8_sdwa v2, v9 src0_sel:BYTE_1
	v_cvt_f32_fp8_sdwa v8, v3 src0_sel:BYTE_1
	v_pk_add_f32 v[18:19], v[18:19], 1.0 op_sel_hi:[1,0]
	v_add_f32_e32 v1, 1.0, v1
	v_pk_mul_f32 v[14:15], v[18:19], v[20:21]
	v_max_f32_e32 v0, 0xc1f00000, v0
	v_pk_mul_f32 v[136:137], v[136:137], v[14:15]
	v_rcp_f32_e32 v14, v1
	v_max_f32_e32 v1, v2, v2
	v_mul_f32_e32 v2, 0xbfb8aa3b, v8
	v_exp_f32_e32 v2, v2
	v_cvt_f32_fp8_sdwa v8, v9 src0_sel:BYTE_2
	v_cvt_f32_fp8_sdwa v9, v9 src0_sel:BYTE_3
	v_max_f32_e32 v1, 0xc1f00000, v1
	v_add_f32_e32 v2, 1.0, v2
	v_rcp_f32_e32 v15, v2
	v_cvt_f32_fp8_sdwa v2, v3 src0_sel:BYTE_2
	v_cvt_f32_fp8_sdwa v3, v3 src0_sel:BYTE_3
	v_max_f32_e32 v8, 0xc1f00000, v8
	v_mul_f32_e32 v2, 0xbfb8aa3b, v2
	v_exp_f32_e32 v17, v2
	v_mul_f32_e32 v8, 0xbfb8aa3b, v8
	v_mul_f32_e32 v3, 0xbfb8aa3b, v3
	v_exp_f32_e32 v2, v8
	v_add_f32_e32 v8, 1.0, v17
	v_exp_f32_e32 v17, v3
	v_max_f32_e32 v9, v9, v9
	v_max_f32_e32 v9, 0xc1f00000, v9
	v_mul_f32_e32 v3, 0xbfb8aa3b, v9
	v_exp_f32_e32 v3, v3
	v_add_f32_e32 v9, 1.0, v17
	v_rcp_f32_e32 v8, v8
	v_rcp_f32_e32 v9, v9
	v_mul_f32_e32 v0, 0xbfb8aa3b, v0
	v_mul_f32_e32 v1, 0xbfb8aa3b, v1
	v_exp_f32_e32 v0, v0
	v_exp_f32_e32 v1, v1
	v_pk_add_f32 v[2:3], v[2:3], 1.0 op_sel_hi:[1,0]
	s_waitcnt vmcnt(0)
	v_cvt_f32_fp8_sdwa v17, v6 src0_sel:BYTE_1
	v_pk_mul_f32 v[2:3], v[2:3], v[8:9]
	v_pk_add_f32 v[0:1], v[0:1], 1.0 op_sel_hi:[1,0]
	v_pk_mul_f32 v[132:133], v[132:133], v[2:3]
	v_cvt_f32_fp8_e32 v2, v4
	v_cvt_f32_fp8_e32 v8, v10
	v_pk_mul_f32 v[0:1], v[0:1], v[14:15]
	v_cvt_f32_fp8_sdwa v9, v4 src0_sel:BYTE_2
	v_pk_mul_f32 v[130:131], v[130:131], v[0:1]
	v_mul_f32_e32 v1, 0xbfb8aa3b, v2
	v_exp_f32_e32 v1, v1
	v_max_f32_e32 v0, v8, v8
	v_cvt_f32_fp8_sdwa v3, v10 src0_sel:BYTE_1
	v_cvt_f32_fp8_sdwa v8, v4 src0_sel:BYTE_1
	v_cvt_f32_fp8_sdwa v4, v4 src0_sel:BYTE_3
	v_add_f32_e32 v1, 1.0, v1
	v_mul_f32_e32 v9, 0xbfb8aa3b, v9
	v_rcp_f32_e32 v2, v1
	v_max_f32_e32 v1, v3, v3
	v_mul_f32_e32 v3, 0xbfb8aa3b, v8
	v_cvt_f32_fp8_sdwa v8, v10 src0_sel:BYTE_2
	v_exp_f32_e32 v9, v9
	v_cvt_f32_fp8_sdwa v10, v10 src0_sel:BYTE_3
	v_mul_f32_e32 v4, 0xbfb8aa3b, v4
	v_exp_f32_e32 v3, v3
	v_exp_f32_e32 v4, v4
	v_max_f32_e32 v8, v8, v8
	v_add_f32_e32 v14, 1.0, v9
	v_max_f32_e32 v9, v10, v10
	v_max_f32_e32 v0, 0xc1f00000, v0
	v_max_f32_e32 v1, 0xc1f00000, v1
	v_max_f32_e32 v8, 0xc1f00000, v8
	v_max_f32_e32 v9, 0xc1f00000, v9
	v_mul_f32_e32 v0, 0xbfb8aa3b, v0
	v_mul_f32_e32 v1, 0xbfb8aa3b, v1
	v_mul_f32_e32 v8, 0xbfb8aa3b, v8
	v_mul_f32_e32 v9, 0xbfb8aa3b, v9
	v_exp_f32_e32 v0, v0
	v_exp_f32_e32 v1, v1
	v_add_f32_e32 v3, 1.0, v3
	v_exp_f32_e32 v8, v8
	v_exp_f32_e32 v9, v9
	v_add_f32_e32 v4, 1.0, v4
	v_rcp_f32_e32 v3, v3
	v_rcp_f32_e32 v14, v14
	v_rcp_f32_e32 v15, v4
	v_pk_add_f32 v[8:9], v[8:9], 1.0 op_sel_hi:[1,0]
	v_pk_add_f32 v[0:1], v[0:1], 1.0 op_sel_hi:[1,0]
	v_cvt_f32_fp8_e32 v4, v11
	v_pk_mul_f32 v[0:1], v[0:1], v[2:3]
	v_pk_mul_f32 v[2:3], v[8:9], v[14:15]
	v_pk_mul_f32 v[126:127], v[126:127], v[0:1]
	v_pk_mul_f32 v[128:129], v[128:129], v[2:3]
	v_cvt_f32_fp8_e32 v2, v5
	v_max_f32_e32 v0, v4, v4
	v_cvt_f32_fp8_sdwa v3, v11 src0_sel:BYTE_1
	v_cvt_f32_fp8_sdwa v4, v5 src0_sel:BYTE_1
	v_mul_f32_e32 v1, 0xbfb8aa3b, v2
	v_exp_f32_e32 v1, v1
	v_cvt_f32_fp8_sdwa v8, v5 src0_sel:BYTE_2
	v_cvt_f32_fp8_sdwa v5, v5 src0_sel:BYTE_3
	v_cvt_f32_fp8_sdwa v9, v11 src0_sel:BYTE_3
	v_add_f32_e32 v1, 1.0, v1
	v_rcp_f32_e32 v2, v1
	v_max_f32_e32 v1, v3, v3
	v_mul_f32_e32 v3, 0xbfb8aa3b, v4
	v_cvt_f32_fp8_sdwa v4, v11 src0_sel:BYTE_2
	v_mul_f32_e32 v8, 0xbfb8aa3b, v8
	v_mul_f32_e32 v5, 0xbfb8aa3b, v5
	v_exp_f32_e32 v3, v3
	v_exp_f32_e32 v8, v8
	v_exp_f32_e32 v10, v5
	v_max_f32_e32 v4, v4, v4
	v_max_f32_e32 v0, 0xc1f00000, v0
	v_max_f32_e32 v1, 0xc1f00000, v1
	v_max_f32_e32 v4, 0xc1f00000, v4
	v_max_f32_e32 v9, 0xc1f00000, v9
	v_mul_f32_e32 v0, 0xbfb8aa3b, v0
	v_mul_f32_e32 v1, 0xbfb8aa3b, v1
	v_mul_f32_e32 v4, 0xbfb8aa3b, v4
	v_mul_f32_e32 v5, 0xbfb8aa3b, v9
	v_exp_f32_e32 v0, v0
	v_exp_f32_e32 v1, v1
	v_add_f32_e32 v3, 1.0, v3
	v_exp_f32_e32 v4, v4
	v_add_f32_e32 v8, 1.0, v8
	v_exp_f32_e32 v5, v5
	v_add_f32_e32 v9, 1.0, v10
	v_rcp_f32_e32 v3, v3
	v_rcp_f32_e32 v8, v8
	v_rcp_f32_e32 v9, v9
	v_pk_add_f32 v[4:5], v[4:5], 1.0 op_sel_hi:[1,0]
	v_pk_add_f32 v[0:1], v[0:1], 1.0 op_sel_hi:[1,0]
	v_cvt_f32_fp8_sdwa v15, v12 src0_sel:BYTE_1
	v_pk_mul_f32 v[0:1], v[0:1], v[2:3]
	v_pk_mul_f32 v[2:3], v[4:5], v[8:9]
	v_cvt_f32_fp8_e32 v5, v6
	v_cvt_f32_fp8_e32 v4, v12
	v_pk_mul_f32 v[122:123], v[122:123], v[0:1]
	v_add_u32_e32 v8, 0x30000, v16
	v_mul_f32_e32 v1, 0xbfb8aa3b, v5
	v_exp_f32_e32 v1, v1
	v_max_f32_e32 v0, v4, v4
	v_max_f32_e32 v0, 0xc1f00000, v0
	v_mul_f32_e32 v0, 0xbfb8aa3b, v0
	v_pk_mul_f32 v[124:125], v[124:125], v[2:3]
	v_exp_f32_e32 v4, v0
	v_add_f32_e32 v5, 1.0, v1
	global_load_dwordx4 v[0:3], v8, s[16:17]
	s_nop 0
	global_load_dwordx4 v[8:11], v8, s[16:17] offset:2048
	v_cvt_f32_fp8_sdwa v18, v6 src0_sel:BYTE_2
	v_cvt_f32_fp8_sdwa v6, v6 src0_sel:BYTE_3
	v_rcp_f32_e32 v14, v5
	v_max_f32_e32 v5, v15, v15
	v_mul_f32_e32 v15, 0xbfb8aa3b, v17
	v_cvt_f32_fp8_sdwa v17, v12 src0_sel:BYTE_2
	v_cvt_f32_fp8_sdwa v12, v12 src0_sel:BYTE_3
	v_exp_f32_e32 v15, v15
	v_mul_f32_e32 v18, 0xbfb8aa3b, v18
	v_max_f32_e32 v5, 0xc1f00000, v5
	v_exp_f32_e32 v19, v18
	v_mul_f32_e32 v6, 0xbfb8aa3b, v6
	v_mul_f32_e32 v5, 0xbfb8aa3b, v5
	v_exp_f32_e32 v6, v6
	v_exp_f32_e32 v5, v5
	v_add_f32_e32 v15, 1.0, v15
	v_max_f32_e32 v17, 0xc1f00000, v17
	v_max_f32_e32 v12, 0xc1f00000, v12
	v_rcp_f32_e32 v15, v15
	v_mul_f32_e32 v17, 0xbfb8aa3b, v17
	v_mul_f32_e32 v12, 0xbfb8aa3b, v12
	v_exp_f32_e32 v18, v17
	v_add_f32_e32 v17, 1.0, v19
	v_exp_f32_e32 v19, v12
	v_cvt_f32_fp8_e32 v12, v7
	v_add_f32_e32 v6, 1.0, v6
	v_rcp_f32_e32 v21, v6
	v_pk_add_f32 v[4:5], v[4:5], 1.0 op_sel_hi:[1,0]
	v_cvt_f32_fp8_e32 v6, v13
	v_pk_mul_f32 v[4:5], v[4:5], v[14:15]
	v_rcp_f32_e32 v20, v17
	v_pk_mul_f32 v[118:119], v[118:119], v[4:5]
	v_mul_f32_e32 v5, 0xbfb8aa3b, v12
	v_exp_f32_e32 v5, v5
	v_max_f32_e32 v4, v6, v6
	v_cvt_f32_fp8_sdwa v6, v13 src0_sel:BYTE_1
	v_cvt_f32_fp8_sdwa v12, v7 src0_sel:BYTE_1
	v_pk_add_f32 v[18:19], v[18:19], 1.0 op_sel_hi:[1,0]
	v_add_f32_e32 v5, 1.0, v5
	v_pk_mul_f32 v[14:15], v[18:19], v[20:21]
	v_max_f32_e32 v4, 0xc1f00000, v4
	v_pk_mul_f32 v[120:121], v[120:121], v[14:15]
	v_rcp_f32_e32 v14, v5
	v_max_f32_e32 v5, v6, v6
	v_mul_f32_e32 v6, 0xbfb8aa3b, v12
	v_exp_f32_e32 v6, v6
	v_cvt_f32_fp8_sdwa v12, v13 src0_sel:BYTE_2
	v_cvt_f32_fp8_sdwa v13, v13 src0_sel:BYTE_3
	v_max_f32_e32 v5, 0xc1f00000, v5
	v_add_f32_e32 v6, 1.0, v6
	v_rcp_f32_e32 v15, v6
	v_cvt_f32_fp8_sdwa v6, v7 src0_sel:BYTE_2
	v_cvt_f32_fp8_sdwa v7, v7 src0_sel:BYTE_3
	v_max_f32_e32 v12, 0xc1f00000, v12
	v_mul_f32_e32 v6, 0xbfb8aa3b, v6
	v_exp_f32_e32 v17, v6
	v_mul_f32_e32 v12, 0xbfb8aa3b, v12
	v_mul_f32_e32 v7, 0xbfb8aa3b, v7
	v_exp_f32_e32 v6, v12
	v_add_f32_e32 v12, 1.0, v17
	v_exp_f32_e32 v17, v7
	v_max_f32_e32 v13, v13, v13
	v_max_f32_e32 v13, 0xc1f00000, v13
	v_mul_f32_e32 v7, 0xbfb8aa3b, v13
	v_exp_f32_e32 v7, v7
	v_add_f32_e32 v13, 1.0, v17
	v_rcp_f32_e32 v12, v12
	v_rcp_f32_e32 v13, v13
	v_mul_f32_e32 v4, 0xbfb8aa3b, v4
	v_mul_f32_e32 v5, 0xbfb8aa3b, v5
	v_exp_f32_e32 v4, v4
	v_exp_f32_e32 v5, v5
	v_pk_add_f32 v[6:7], v[6:7], 1.0 op_sel_hi:[1,0]
	v_pk_add_f32 v[4:5], v[4:5], 1.0 op_sel_hi:[1,0]
	v_pk_mul_f32 v[6:7], v[6:7], v[12:13]
	s_waitcnt vmcnt(0)
	v_cvt_f32_fp8_e32 v12, v8
	v_pk_mul_f32 v[116:117], v[116:117], v[6:7]
	v_cvt_f32_fp8_e32 v6, v0
	v_pk_mul_f32 v[4:5], v[4:5], v[14:15]
	v_cvt_f32_fp8_sdwa v7, v8 src0_sel:BYTE_1
	v_pk_mul_f32 v[114:115], v[114:115], v[4:5]
	v_mul_f32_e32 v5, 0xbfb8aa3b, v6
	v_exp_f32_e32 v5, v5
	v_max_f32_e32 v4, v12, v12
	v_cvt_f32_fp8_sdwa v12, v0 src0_sel:BYTE_1
	v_cvt_f32_fp8_sdwa v13, v0 src0_sel:BYTE_2
	v_cvt_f32_fp8_sdwa v0, v0 src0_sel:BYTE_3
	v_add_f32_e32 v5, 1.0, v5
	v_rcp_f32_e32 v6, v5
	v_max_f32_e32 v5, v7, v7
	v_mul_f32_e32 v7, 0xbfb8aa3b, v12
	v_cvt_f32_fp8_sdwa v12, v8 src0_sel:BYTE_2
	v_cvt_f32_fp8_sdwa v8, v8 src0_sel:BYTE_3
	v_mul_f32_e32 v13, 0xbfb8aa3b, v13
	v_mul_f32_e32 v0, 0xbfb8aa3b, v0
	v_exp_f32_e32 v7, v7
	v_exp_f32_e32 v13, v13
	v_exp_f32_e32 v0, v0
	v_max_f32_e32 v12, v12, v12
	v_max_f32_e32 v4, 0xc1f00000, v4
	v_max_f32_e32 v5, 0xc1f00000, v5
	v_max_f32_e32 v12, 0xc1f00000, v12
	v_max_f32_e32 v8, 0xc1f00000, v8
	v_mul_f32_e32 v4, 0xbfb8aa3b, v4
	v_mul_f32_e32 v5, 0xbfb8aa3b, v5
	v_mul_f32_e32 v12, 0xbfb8aa3b, v12
	v_mul_f32_e32 v8, 0xbfb8aa3b, v8
	v_exp_f32_e32 v4, v4
	v_exp_f32_e32 v5, v5
	v_add_f32_e32 v7, 1.0, v7
	v_exp_f32_e32 v12, v12
	v_add_f32_e32 v14, 1.0, v13
	v_exp_f32_e32 v13, v8
	v_add_f32_e32 v0, 1.0, v0
	v_rcp_f32_e32 v7, v7
	v_rcp_f32_e32 v14, v14
	v_rcp_f32_e32 v15, v0
	v_pk_add_f32 v[12:13], v[12:13], 1.0 op_sel_hi:[1,0]
	v_pk_add_f32 v[4:5], v[4:5], 1.0 op_sel_hi:[1,0]
	v_cvt_f32_fp8_e32 v0, v9
	v_pk_mul_f32 v[4:5], v[4:5], v[6:7]
	v_pk_mul_f32 v[6:7], v[12:13], v[14:15]
	v_pk_mul_f32 v[110:111], v[110:111], v[4:5]
	v_pk_mul_f32 v[112:113], v[112:113], v[6:7]
	v_cvt_f32_fp8_e32 v6, v1
	v_max_f32_e32 v0, 0xc1f00000, v0
	v_mul_f32_e32 v0, 0xbfb8aa3b, v0
	v_mul_f32_e32 v4, 0xbfb8aa3b, v6
	v_exp_f32_e32 v5, v4
	v_exp_f32_e32 v4, v0
	v_cvt_f32_fp8_sdwa v0, v9 src0_sel:BYTE_1
	v_cvt_f32_fp8_sdwa v7, v1 src0_sel:BYTE_1
	v_add_f32_e32 v5, 1.0, v5
	v_cvt_f32_fp8_sdwa v8, v1 src0_sel:BYTE_2
	v_max_f32_e32 v0, 0xc1f00000, v0
	v_cvt_f32_fp8_sdwa v1, v1 src0_sel:BYTE_3
	v_rcp_f32_e32 v6, v5
	v_mul_f32_e32 v5, 0xbfb8aa3b, v7
	v_mul_f32_e32 v0, 0xbfb8aa3b, v0
	v_exp_f32_e32 v7, v5
	v_exp_f32_e32 v5, v0
	v_cvt_f32_fp8_sdwa v0, v9 src0_sel:BYTE_2
	v_cvt_f32_fp8_sdwa v9, v9 src0_sel:BYTE_3
	v_mul_f32_e32 v8, 0xbfb8aa3b, v8
	v_mul_f32_e32 v1, 0xbfb8aa3b, v1
	v_exp_f32_e32 v8, v8
	v_exp_f32_e32 v12, v1
	v_add_f32_e32 v7, 1.0, v7
	v_rcp_f32_e32 v7, v7
	v_max_f32_e32 v0, 0xc1f00000, v0
	v_max_f32_e32 v9, 0xc1f00000, v9
	v_mul_f32_e32 v0, 0xbfb8aa3b, v0
	v_mul_f32_e32 v1, 0xbfb8aa3b, v9
	v_exp_f32_e32 v0, v0
	v_add_f32_e32 v8, 1.0, v8
	v_exp_f32_e32 v1, v1
	v_add_f32_e32 v9, 1.0, v12
	v_rcp_f32_e32 v8, v8
	v_rcp_f32_e32 v9, v9
	v_pk_add_f32 v[4:5], v[4:5], 1.0 op_sel_hi:[1,0]
	v_pk_add_f32 v[0:1], v[0:1], 1.0 op_sel_hi:[1,0]
	v_pk_mul_f32 v[4:5], v[4:5], v[6:7]
	v_cvt_f32_fp8_e32 v6, v10
	v_cvt_f32_fp8_e32 v7, v2
	v_pk_mul_f32 v[0:1], v[0:1], v[8:9]
	v_add_u32_e32 v8, 0x80000, v16
	v_pk_mul_f32 v[108:109], v[108:109], v[0:1]
	v_pk_mul_f32 v[106:107], v[106:107], v[4:5]
	v_max_f32_e32 v0, v6, v6
	v_mul_f32_e32 v1, 0xbfb8aa3b, v7
	global_load_dwordx4 v[4:7], v8, s[16:17]
	global_load_dwordx4 v[12:15], v8, s[16:17] offset:2048
	v_exp_f32_e32 v1, v1
	v_cvt_f32_fp8_sdwa v9, v10 src0_sel:BYTE_1
	v_cvt_f32_fp8_sdwa v17, v2 src0_sel:BYTE_1
	v_cvt_f32_fp8_sdwa v18, v2 src0_sel:BYTE_2
	v_cvt_f32_fp8_sdwa v2, v2 src0_sel:BYTE_3
	v_add_f32_e32 v1, 1.0, v1
	v_rcp_f32_e32 v8, v1
	v_max_f32_e32 v1, v9, v9
	v_mul_f32_e32 v9, 0xbfb8aa3b, v17
	v_cvt_f32_fp8_sdwa v17, v10 src0_sel:BYTE_2
	v_cvt_f32_fp8_sdwa v10, v10 src0_sel:BYTE_3
	v_mul_f32_e32 v18, 0xbfb8aa3b, v18
	v_mul_f32_e32 v2, 0xbfb8aa3b, v2
	v_exp_f32_e32 v9, v9
	v_exp_f32_e32 v19, v18
	v_exp_f32_e32 v2, v2
	v_max_f32_e32 v17, v17, v17
	v_max_f32_e32 v0, 0xc1f00000, v0
	v_max_f32_e32 v1, 0xc1f00000, v1
	v_max_f32_e32 v17, 0xc1f00000, v17
	v_max_f32_e32 v10, 0xc1f00000, v10
	v_mul_f32_e32 v0, 0xbfb8aa3b, v0
	v_mul_f32_e32 v1, 0xbfb8aa3b, v1
	v_mul_f32_e32 v17, 0xbfb8aa3b, v17
	v_mul_f32_e32 v10, 0xbfb8aa3b, v10
	v_exp_f32_e32 v0, v0
	v_exp_f32_e32 v1, v1
	v_add_f32_e32 v9, 1.0, v9
	v_exp_f32_e32 v18, v17
	v_add_f32_e32 v17, 1.0, v19
	v_exp_f32_e32 v19, v10
	v_add_f32_e32 v2, 1.0, v2
	v_rcp_f32_e32 v9, v9
	v_rcp_f32_e32 v20, v17
	v_rcp_f32_e32 v21, v2
	v_pk_add_f32 v[18:19], v[18:19], 1.0 op_sel_hi:[1,0]
	v_pk_add_f32 v[0:1], v[0:1], 1.0 op_sel_hi:[1,0]
	v_cvt_f32_fp8_e32 v2, v11
	v_pk_mul_f32 v[0:1], v[0:1], v[8:9]
	v_pk_mul_f32 v[8:9], v[18:19], v[20:21]
	v_pk_mul_f32 v[102:103], v[102:103], v[0:1]
	v_pk_mul_f32 v[104:105], v[104:105], v[8:9]
	v_cvt_f32_fp8_e32 v8, v3
	v_max_f32_e32 v0, v2, v2
	v_cvt_f32_fp8_sdwa v2, v11 src0_sel:BYTE_1
	v_cvt_f32_fp8_sdwa v9, v3 src0_sel:BYTE_1
	v_mul_f32_e32 v1, 0xbfb8aa3b, v8
	v_exp_f32_e32 v1, v1
	v_cvt_f32_fp8_sdwa v10, v11 src0_sel:BYTE_2
	v_cvt_f32_fp8_sdwa v11, v11 src0_sel:BYTE_3
	v_max_f32_e32 v0, 0xc1f00000, v0
	v_add_f32_e32 v1, 1.0, v1
	v_rcp_f32_e32 v8, v1
	v_max_f32_e32 v1, v2, v2
	v_mul_f32_e32 v2, 0xbfb8aa3b, v9
	v_exp_f32_e32 v2, v2
	v_max_f32_e32 v10, v10, v10
	v_max_f32_e32 v10, 0xc1f00000, v10
	v_mul_f32_e32 v10, 0xbfb8aa3b, v10
	v_add_f32_e32 v2, 1.0, v2
	v_rcp_f32_e32 v9, v2
	v_cvt_f32_fp8_sdwa v2, v3 src0_sel:BYTE_2
	v_cvt_f32_fp8_sdwa v3, v3 src0_sel:BYTE_3
	v_max_f32_e32 v11, 0xc1f00000, v11
	v_mul_f32_e32 v2, 0xbfb8aa3b, v2
	v_exp_f32_e32 v17, v2
	v_mul_f32_e32 v3, 0xbfb8aa3b, v3
	v_exp_f32_e32 v2, v10
	v_max_f32_e32 v1, 0xc1f00000, v1
	v_add_f32_e32 v10, 1.0, v17
	v_exp_f32_e32 v17, v3
	v_mul_f32_e32 v3, 0xbfb8aa3b, v11
	v_exp_f32_e32 v3, v3
	v_rcp_f32_e32 v10, v10
	v_add_f32_e32 v11, 1.0, v17
	v_rcp_f32_e32 v11, v11
	v_mul_f32_e32 v0, 0xbfb8aa3b, v0
	v_mul_f32_e32 v1, 0xbfb8aa3b, v1
	v_exp_f32_e32 v0, v0
	v_exp_f32_e32 v1, v1
	v_pk_add_f32 v[2:3], v[2:3], 1.0 op_sel_hi:[1,0]
	s_waitcnt vmcnt(0)
	v_cvt_f32_fp8_sdwa v17, v6 src0_sel:BYTE_1
	v_pk_mul_f32 v[2:3], v[2:3], v[10:11]
	v_pk_add_f32 v[0:1], v[0:1], 1.0 op_sel_hi:[1,0]
	v_pk_mul_f32 v[100:101], v[100:101], v[2:3]
	v_cvt_f32_fp8_e32 v2, v4
	v_pk_mul_f32 v[0:1], v[0:1], v[8:9]
	v_cvt_f32_fp8_e32 v8, v12
	v_pk_mul_f32 v[98:99], v[98:99], v[0:1]
	v_mul_f32_e32 v1, 0xbfb8aa3b, v2
	v_exp_f32_e32 v1, v1
	v_cvt_f32_fp8_sdwa v9, v4 src0_sel:BYTE_2
	v_max_f32_e32 v0, v8, v8
	v_cvt_f32_fp8_sdwa v3, v12 src0_sel:BYTE_1
	v_cvt_f32_fp8_sdwa v8, v4 src0_sel:BYTE_1
	v_cvt_f32_fp8_sdwa v4, v4 src0_sel:BYTE_3
	v_add_f32_e32 v1, 1.0, v1
	v_mul_f32_e32 v9, 0xbfb8aa3b, v9
	v_rcp_f32_e32 v2, v1
	v_max_f32_e32 v1, v3, v3
	v_mul_f32_e32 v3, 0xbfb8aa3b, v8
	v_cvt_f32_fp8_sdwa v8, v12 src0_sel:BYTE_2
	v_exp_f32_e32 v9, v9
	v_cvt_f32_fp8_sdwa v10, v12 src0_sel:BYTE_3
	v_mul_f32_e32 v4, 0xbfb8aa3b, v4
	v_exp_f32_e32 v3, v3
	v_exp_f32_e32 v4, v4
	v_max_f32_e32 v8, v8, v8
	v_add_f32_e32 v11, 1.0, v9
	v_max_f32_e32 v9, v10, v10
	v_max_f32_e32 v0, 0xc1f00000, v0
	v_max_f32_e32 v1, 0xc1f00000, v1
	v_max_f32_e32 v8, 0xc1f00000, v8
	v_max_f32_e32 v9, 0xc1f00000, v9
	v_mul_f32_e32 v0, 0xbfb8aa3b, v0
	v_mul_f32_e32 v1, 0xbfb8aa3b, v1
	v_mul_f32_e32 v8, 0xbfb8aa3b, v8
	v_mul_f32_e32 v9, 0xbfb8aa3b, v9
	v_exp_f32_e32 v0, v0
	v_exp_f32_e32 v1, v1
	v_add_f32_e32 v3, 1.0, v3
	v_exp_f32_e32 v8, v8
	v_exp_f32_e32 v9, v9
	v_add_f32_e32 v4, 1.0, v4
	v_rcp_f32_e32 v3, v3
	v_rcp_f32_e32 v10, v11
	v_rcp_f32_e32 v11, v4
	v_pk_add_f32 v[8:9], v[8:9], 1.0 op_sel_hi:[1,0]
	v_pk_add_f32 v[0:1], v[0:1], 1.0 op_sel_hi:[1,0]
	v_cvt_f32_fp8_e32 v4, v13
	v_pk_mul_f32 v[0:1], v[0:1], v[2:3]
	v_pk_mul_f32 v[2:3], v[8:9], v[10:11]
	v_pk_mul_f32 v[94:95], v[94:95], v[0:1]
	v_pk_mul_f32 v[96:97], v[96:97], v[2:3]
	v_cvt_f32_fp8_e32 v2, v5
	v_max_f32_e32 v0, v4, v4
	v_cvt_f32_fp8_sdwa v3, v13 src0_sel:BYTE_1
	v_cvt_f32_fp8_sdwa v4, v5 src0_sel:BYTE_1
	v_mul_f32_e32 v1, 0xbfb8aa3b, v2
	v_exp_f32_e32 v1, v1
	v_cvt_f32_fp8_sdwa v8, v5 src0_sel:BYTE_2
	v_cvt_f32_fp8_sdwa v5, v5 src0_sel:BYTE_3
	v_cvt_f32_fp8_sdwa v9, v13 src0_sel:BYTE_3
	v_add_f32_e32 v1, 1.0, v1
	v_rcp_f32_e32 v2, v1
	v_max_f32_e32 v1, v3, v3
	v_mul_f32_e32 v3, 0xbfb8aa3b, v4
	v_cvt_f32_fp8_sdwa v4, v13 src0_sel:BYTE_2
	v_mul_f32_e32 v8, 0xbfb8aa3b, v8
	v_mul_f32_e32 v5, 0xbfb8aa3b, v5
	v_exp_f32_e32 v3, v3
	v_exp_f32_e32 v8, v8
	v_exp_f32_e32 v10, v5
	v_max_f32_e32 v4, v4, v4
	v_max_f32_e32 v0, 0xc1f00000, v0
	v_max_f32_e32 v1, 0xc1f00000, v1
	v_max_f32_e32 v4, 0xc1f00000, v4
	v_max_f32_e32 v9, 0xc1f00000, v9
	v_mul_f32_e32 v0, 0xbfb8aa3b, v0
	v_mul_f32_e32 v1, 0xbfb8aa3b, v1
	v_mul_f32_e32 v4, 0xbfb8aa3b, v4
	v_mul_f32_e32 v5, 0xbfb8aa3b, v9
	v_exp_f32_e32 v0, v0
	v_exp_f32_e32 v1, v1
	v_add_f32_e32 v3, 1.0, v3
	v_exp_f32_e32 v4, v4
	v_add_f32_e32 v8, 1.0, v8
	v_exp_f32_e32 v5, v5
	v_add_f32_e32 v9, 1.0, v10
	v_rcp_f32_e32 v3, v3
	v_rcp_f32_e32 v8, v8
	v_rcp_f32_e32 v9, v9
	v_pk_add_f32 v[4:5], v[4:5], 1.0 op_sel_hi:[1,0]
	v_pk_add_f32 v[0:1], v[0:1], 1.0 op_sel_hi:[1,0]
	v_cvt_f32_fp8_sdwa v13, v14 src0_sel:BYTE_1
	v_pk_mul_f32 v[0:1], v[0:1], v[2:3]
	v_pk_mul_f32 v[2:3], v[4:5], v[8:9]
	v_cvt_f32_fp8_e32 v5, v6
	v_cvt_f32_fp8_e32 v4, v14
	v_pk_mul_f32 v[90:91], v[90:91], v[0:1]
	v_add_u32_e32 v8, 0x90000, v16
	v_mul_f32_e32 v1, 0xbfb8aa3b, v5
	v_exp_f32_e32 v1, v1
	v_max_f32_e32 v0, v4, v4
	v_max_f32_e32 v0, 0xc1f00000, v0
	v_mul_f32_e32 v0, 0xbfb8aa3b, v0
	v_pk_mul_f32 v[92:93], v[92:93], v[2:3]
	v_exp_f32_e32 v4, v0
	v_add_f32_e32 v5, 1.0, v1
	global_load_dwordx4 v[0:3], v8, s[16:17]
	s_nop 0
	global_load_dwordx4 v[8:11], v8, s[16:17] offset:2048
	v_cvt_f32_fp8_sdwa v18, v6 src0_sel:BYTE_2
	v_cvt_f32_fp8_sdwa v6, v6 src0_sel:BYTE_3
	v_rcp_f32_e32 v12, v5
	v_max_f32_e32 v5, v13, v13
	v_mul_f32_e32 v13, 0xbfb8aa3b, v17
	v_cvt_f32_fp8_sdwa v17, v14 src0_sel:BYTE_2
	v_cvt_f32_fp8_sdwa v14, v14 src0_sel:BYTE_3
	v_mul_f32_e32 v18, 0xbfb8aa3b, v18
	v_mul_f32_e32 v6, 0xbfb8aa3b, v6
	v_exp_f32_e32 v13, v13
	v_exp_f32_e32 v19, v18
	v_exp_f32_e32 v6, v6
	v_max_f32_e32 v17, v17, v17
	v_max_f32_e32 v5, 0xc1f00000, v5
	v_max_f32_e32 v17, 0xc1f00000, v17
	v_max_f32_e32 v14, 0xc1f00000, v14
	v_mul_f32_e32 v5, 0xbfb8aa3b, v5
	v_mul_f32_e32 v17, 0xbfb8aa3b, v17
	v_mul_f32_e32 v14, 0xbfb8aa3b, v14
	v_exp_f32_e32 v5, v5
	v_add_f32_e32 v13, 1.0, v13
	v_exp_f32_e32 v18, v17
	v_add_f32_e32 v17, 1.0, v19
	v_exp_f32_e32 v19, v14
	v_add_f32_e32 v6, 1.0, v6
	v_rcp_f32_e32 v13, v13
	v_rcp_f32_e32 v20, v17
	v_rcp_f32_e32 v21, v6
	v_pk_add_f32 v[18:19], v[18:19], 1.0 op_sel_hi:[1,0]
	v_pk_add_f32 v[4:5], v[4:5], 1.0 op_sel_hi:[1,0]
	v_cvt_f32_fp8_e32 v6, v15
	v_pk_mul_f32 v[4:5], v[4:5], v[12:13]
	v_pk_mul_f32 v[12:13], v[18:19], v[20:21]
	v_pk_mul_f32 v[86:87], v[86:87], v[4:5]
	v_pk_mul_f32 v[88:89], v[88:89], v[12:13]
	v_cvt_f32_fp8_e32 v12, v7
	v_max_f32_e32 v4, v6, v6
	v_cvt_f32_fp8_sdwa v6, v15 src0_sel:BYTE_1
	v_cvt_f32_fp8_sdwa v13, v7 src0_sel:BYTE_1
	v_mul_f32_e32 v5, 0xbfb8aa3b, v12
	v_exp_f32_e32 v5, v5
	v_cvt_f32_fp8_sdwa v14, v15 src0_sel:BYTE_2
	v_cvt_f32_fp8_sdwa v15, v15 src0_sel:BYTE_3
	v_max_f32_e32 v4, 0xc1f00000, v4
	v_add_f32_e32 v5, 1.0, v5
	v_rcp_f32_e32 v12, v5
	v_max_f32_e32 v5, v6, v6
	v_mul_f32_e32 v6, 0xbfb8aa3b, v13
	v_exp_f32_e32 v6, v6
	v_max_f32_e32 v14, v14, v14
	v_max_f32_e32 v14, 0xc1f00000, v14
	v_mul_f32_e32 v14, 0xbfb8aa3b, v14
	v_add_f32_e32 v6, 1.0, v6
	v_rcp_f32_e32 v13, v6
	v_cvt_f32_fp8_sdwa v6, v7 src0_sel:BYTE_2
	v_cvt_f32_fp8_sdwa v7, v7 src0_sel:BYTE_3
	v_max_f32_e32 v15, 0xc1f00000, v15
	v_mul_f32_e32 v6, 0xbfb8aa3b, v6
	v_exp_f32_e32 v17, v6
	v_mul_f32_e32 v7, 0xbfb8aa3b, v7
	v_exp_f32_e32 v6, v14
	v_max_f32_e32 v5, 0xc1f00000, v5
	v_add_f32_e32 v14, 1.0, v17
	v_exp_f32_e32 v17, v7
	v_mul_f32_e32 v7, 0xbfb8aa3b, v15
	v_exp_f32_e32 v7, v7
	v_rcp_f32_e32 v14, v14
	v_add_f32_e32 v15, 1.0, v17
	v_rcp_f32_e32 v15, v15
	v_mul_f32_e32 v4, 0xbfb8aa3b, v4
	v_mul_f32_e32 v5, 0xbfb8aa3b, v5
	v_exp_f32_e32 v4, v4
	v_exp_f32_e32 v5, v5
	v_pk_add_f32 v[6:7], v[6:7], 1.0 op_sel_hi:[1,0]
	v_pk_add_f32 v[4:5], v[4:5], 1.0 op_sel_hi:[1,0]
	v_pk_mul_f32 v[6:7], v[6:7], v[14:15]
	v_pk_mul_f32 v[4:5], v[4:5], v[12:13]
	v_pk_mul_f32 v[84:85], v[84:85], v[6:7]
	s_waitcnt vmcnt(0)
	v_cvt_f32_fp8_e32 v6, v0
	v_cvt_f32_fp8_e32 v12, v8
	v_pk_mul_f32 v[82:83], v[82:83], v[4:5]
	v_cvt_f32_fp8_sdwa v7, v8 src0_sel:BYTE_1
	v_mul_f32_e32 v5, 0xbfb8aa3b, v6
	v_exp_f32_e32 v5, v5
	v_max_f32_e32 v4, v12, v12
	v_cvt_f32_fp8_sdwa v12, v0 src0_sel:BYTE_1
	v_cvt_f32_fp8_sdwa v13, v0 src0_sel:BYTE_2
	v_cvt_f32_fp8_sdwa v0, v0 src0_sel:BYTE_3
	v_add_f32_e32 v5, 1.0, v5
	v_rcp_f32_e32 v6, v5
	v_max_f32_e32 v5, v7, v7
	v_mul_f32_e32 v7, 0xbfb8aa3b, v12
	v_cvt_f32_fp8_sdwa v12, v8 src0_sel:BYTE_2
	v_cvt_f32_fp8_sdwa v8, v8 src0_sel:BYTE_3
	v_mul_f32_e32 v13, 0xbfb8aa3b, v13
	v_mul_f32_e32 v0, 0xbfb8aa3b, v0
	v_exp_f32_e32 v7, v7
	v_exp_f32_e32 v13, v13
	v_exp_f32_e32 v0, v0
	v_max_f32_e32 v12, v12, v12
	v_max_f32_e32 v4, 0xc1f00000, v4
	v_max_f32_e32 v5, 0xc1f00000, v5
	v_max_f32_e32 v12, 0xc1f00000, v12
	v_max_f32_e32 v8, 0xc1f00000, v8
	v_mul_f32_e32 v4, 0xbfb8aa3b, v4
	v_mul_f32_e32 v5, 0xbfb8aa3b, v5
	v_mul_f32_e32 v12, 0xbfb8aa3b, v12
	v_mul_f32_e32 v8, 0xbfb8aa3b, v8
	v_exp_f32_e32 v4, v4
	v_exp_f32_e32 v5, v5
	v_add_f32_e32 v7, 1.0, v7
	v_exp_f32_e32 v12, v12
	v_add_f32_e32 v14, 1.0, v13
	v_exp_f32_e32 v13, v8
	v_add_f32_e32 v0, 1.0, v0
	v_rcp_f32_e32 v7, v7
	v_rcp_f32_e32 v14, v14
	v_rcp_f32_e32 v15, v0
	v_pk_add_f32 v[12:13], v[12:13], 1.0 op_sel_hi:[1,0]
	v_pk_add_f32 v[4:5], v[4:5], 1.0 op_sel_hi:[1,0]
	v_cvt_f32_fp8_e32 v0, v9
	v_pk_mul_f32 v[4:5], v[4:5], v[6:7]
	v_pk_mul_f32 v[6:7], v[12:13], v[14:15]
	v_pk_mul_f32 v[78:79], v[78:79], v[4:5]
	v_pk_mul_f32 v[80:81], v[80:81], v[6:7]
	v_cvt_f32_fp8_e32 v6, v1
	v_max_f32_e32 v0, 0xc1f00000, v0
	v_mul_f32_e32 v0, 0xbfb8aa3b, v0
	v_mul_f32_e32 v4, 0xbfb8aa3b, v6
	v_exp_f32_e32 v5, v4
	v_exp_f32_e32 v4, v0
	v_cvt_f32_fp8_sdwa v0, v9 src0_sel:BYTE_1
	v_cvt_f32_fp8_sdwa v7, v1 src0_sel:BYTE_1
	v_add_f32_e32 v5, 1.0, v5
	v_cvt_f32_fp8_sdwa v8, v1 src0_sel:BYTE_2
	v_max_f32_e32 v0, 0xc1f00000, v0
	v_cvt_f32_fp8_sdwa v1, v1 src0_sel:BYTE_3
	v_rcp_f32_e32 v6, v5
	v_mul_f32_e32 v5, 0xbfb8aa3b, v7
	v_mul_f32_e32 v0, 0xbfb8aa3b, v0
	v_exp_f32_e32 v7, v5
	v_exp_f32_e32 v5, v0
	v_cvt_f32_fp8_sdwa v0, v9 src0_sel:BYTE_2
	v_cvt_f32_fp8_sdwa v9, v9 src0_sel:BYTE_3
	v_mul_f32_e32 v8, 0xbfb8aa3b, v8
	v_mul_f32_e32 v1, 0xbfb8aa3b, v1
	v_exp_f32_e32 v8, v8
	v_exp_f32_e32 v12, v1
	v_add_f32_e32 v7, 1.0, v7
	v_rcp_f32_e32 v7, v7
	v_max_f32_e32 v0, 0xc1f00000, v0
	v_max_f32_e32 v9, 0xc1f00000, v9
	v_mul_f32_e32 v0, 0xbfb8aa3b, v0
	v_mul_f32_e32 v1, 0xbfb8aa3b, v9
	v_exp_f32_e32 v0, v0
	v_add_f32_e32 v8, 1.0, v8
	v_exp_f32_e32 v1, v1
	v_add_f32_e32 v9, 1.0, v12
	v_rcp_f32_e32 v8, v8
	v_rcp_f32_e32 v9, v9
	v_pk_add_f32 v[4:5], v[4:5], 1.0 op_sel_hi:[1,0]
	v_pk_add_f32 v[0:1], v[0:1], 1.0 op_sel_hi:[1,0]
	v_pk_mul_f32 v[4:5], v[4:5], v[6:7]
	v_cvt_f32_fp8_e32 v6, v10
	v_cvt_f32_fp8_e32 v7, v2
	v_pk_mul_f32 v[0:1], v[0:1], v[8:9]
	v_add_u32_e32 v8, 0xa0000, v16
	v_pk_mul_f32 v[76:77], v[76:77], v[0:1]
	v_pk_mul_f32 v[74:75], v[74:75], v[4:5]
	v_max_f32_e32 v0, v6, v6
	v_mul_f32_e32 v1, 0xbfb8aa3b, v7
	global_load_dwordx4 v[4:7], v8, s[16:17]
	global_load_dwordx4 v[12:15], v8, s[16:17] offset:2048
	v_exp_f32_e32 v1, v1
	v_cvt_f32_fp8_sdwa v9, v10 src0_sel:BYTE_1
	v_cvt_f32_fp8_sdwa v17, v2 src0_sel:BYTE_1
	v_cvt_f32_fp8_sdwa v18, v2 src0_sel:BYTE_2
	v_cvt_f32_fp8_sdwa v2, v2 src0_sel:BYTE_3
	v_add_f32_e32 v1, 1.0, v1
	v_rcp_f32_e32 v8, v1
	v_max_f32_e32 v1, v9, v9
	v_mul_f32_e32 v9, 0xbfb8aa3b, v17
	v_cvt_f32_fp8_sdwa v17, v10 src0_sel:BYTE_2
	v_cvt_f32_fp8_sdwa v10, v10 src0_sel:BYTE_3
	v_mul_f32_e32 v18, 0xbfb8aa3b, v18
	v_mul_f32_e32 v2, 0xbfb8aa3b, v2
	v_exp_f32_e32 v9, v9
	v_exp_f32_e32 v19, v18
	v_exp_f32_e32 v2, v2
	v_max_f32_e32 v17, v17, v17
	v_max_f32_e32 v0, 0xc1f00000, v0
	v_max_f32_e32 v1, 0xc1f00000, v1
	v_max_f32_e32 v17, 0xc1f00000, v17
	v_max_f32_e32 v10, 0xc1f00000, v10
	v_mul_f32_e32 v0, 0xbfb8aa3b, v0
	v_mul_f32_e32 v1, 0xbfb8aa3b, v1
	v_mul_f32_e32 v17, 0xbfb8aa3b, v17
	v_mul_f32_e32 v10, 0xbfb8aa3b, v10
	v_exp_f32_e32 v0, v0
	v_exp_f32_e32 v1, v1
	v_add_f32_e32 v9, 1.0, v9
	v_exp_f32_e32 v18, v17
	v_add_f32_e32 v17, 1.0, v19
	v_exp_f32_e32 v19, v10
	v_add_f32_e32 v2, 1.0, v2
	v_rcp_f32_e32 v9, v9
	v_rcp_f32_e32 v20, v17
	v_rcp_f32_e32 v21, v2
	v_pk_add_f32 v[18:19], v[18:19], 1.0 op_sel_hi:[1,0]
	v_pk_add_f32 v[0:1], v[0:1], 1.0 op_sel_hi:[1,0]
	v_cvt_f32_fp8_e32 v2, v11
	v_pk_mul_f32 v[0:1], v[0:1], v[8:9]
	v_pk_mul_f32 v[8:9], v[18:19], v[20:21]
	v_pk_mul_f32 v[70:71], v[70:71], v[0:1]
	v_pk_mul_f32 v[72:73], v[72:73], v[8:9]
	v_cvt_f32_fp8_e32 v8, v3
	v_max_f32_e32 v0, v2, v2
	v_cvt_f32_fp8_sdwa v2, v11 src0_sel:BYTE_1
	v_cvt_f32_fp8_sdwa v9, v3 src0_sel:BYTE_1
	v_mul_f32_e32 v1, 0xbfb8aa3b, v8
	v_exp_f32_e32 v1, v1
	v_cvt_f32_fp8_sdwa v10, v11 src0_sel:BYTE_2
	v_cvt_f32_fp8_sdwa v11, v11 src0_sel:BYTE_3
	v_max_f32_e32 v0, 0xc1f00000, v0
	v_add_f32_e32 v1, 1.0, v1
	v_rcp_f32_e32 v8, v1
	v_max_f32_e32 v1, v2, v2
	v_mul_f32_e32 v2, 0xbfb8aa3b, v9
	v_exp_f32_e32 v2, v2
	v_max_f32_e32 v10, v10, v10
	v_max_f32_e32 v10, 0xc1f00000, v10
	v_mul_f32_e32 v10, 0xbfb8aa3b, v10
	v_add_f32_e32 v2, 1.0, v2
	v_rcp_f32_e32 v9, v2
	v_cvt_f32_fp8_sdwa v2, v3 src0_sel:BYTE_2
	v_cvt_f32_fp8_sdwa v3, v3 src0_sel:BYTE_3
	v_max_f32_e32 v11, 0xc1f00000, v11
	v_mul_f32_e32 v2, 0xbfb8aa3b, v2
	v_exp_f32_e32 v17, v2
	v_mul_f32_e32 v3, 0xbfb8aa3b, v3
	v_exp_f32_e32 v2, v10
	v_max_f32_e32 v1, 0xc1f00000, v1
	v_add_f32_e32 v10, 1.0, v17
	v_exp_f32_e32 v17, v3
	v_mul_f32_e32 v3, 0xbfb8aa3b, v11
	v_exp_f32_e32 v3, v3
	v_rcp_f32_e32 v10, v10
	v_add_f32_e32 v11, 1.0, v17
	v_rcp_f32_e32 v11, v11
	v_mul_f32_e32 v0, 0xbfb8aa3b, v0
	v_mul_f32_e32 v1, 0xbfb8aa3b, v1
	v_exp_f32_e32 v0, v0
	v_exp_f32_e32 v1, v1
	v_pk_add_f32 v[2:3], v[2:3], 1.0 op_sel_hi:[1,0]
	s_waitcnt vmcnt(0)
	v_cvt_f32_fp8_sdwa v17, v6 src0_sel:BYTE_1
	v_pk_mul_f32 v[2:3], v[2:3], v[10:11]
	v_pk_add_f32 v[0:1], v[0:1], 1.0 op_sel_hi:[1,0]
	v_pk_mul_f32 v[68:69], v[68:69], v[2:3]
	v_cvt_f32_fp8_e32 v2, v4
	v_pk_mul_f32 v[0:1], v[0:1], v[8:9]
	v_cvt_f32_fp8_e32 v8, v12
	v_pk_mul_f32 v[66:67], v[66:67], v[0:1]
	v_mul_f32_e32 v1, 0xbfb8aa3b, v2
	v_exp_f32_e32 v1, v1
	v_cvt_f32_fp8_sdwa v9, v4 src0_sel:BYTE_2
	v_max_f32_e32 v0, v8, v8
	v_cvt_f32_fp8_sdwa v3, v12 src0_sel:BYTE_1
	v_cvt_f32_fp8_sdwa v8, v4 src0_sel:BYTE_1
	v_cvt_f32_fp8_sdwa v4, v4 src0_sel:BYTE_3
	v_add_f32_e32 v1, 1.0, v1
	v_mul_f32_e32 v9, 0xbfb8aa3b, v9
	v_rcp_f32_e32 v2, v1
	v_max_f32_e32 v1, v3, v3
	v_mul_f32_e32 v3, 0xbfb8aa3b, v8
	v_cvt_f32_fp8_sdwa v8, v12 src0_sel:BYTE_2
	v_exp_f32_e32 v9, v9
	v_cvt_f32_fp8_sdwa v10, v12 src0_sel:BYTE_3
	v_mul_f32_e32 v4, 0xbfb8aa3b, v4
	v_exp_f32_e32 v3, v3
	v_exp_f32_e32 v4, v4
	v_max_f32_e32 v8, v8, v8
	v_add_f32_e32 v11, 1.0, v9
	v_max_f32_e32 v9, v10, v10
	v_max_f32_e32 v0, 0xc1f00000, v0
	v_max_f32_e32 v1, 0xc1f00000, v1
	v_max_f32_e32 v8, 0xc1f00000, v8
	v_max_f32_e32 v9, 0xc1f00000, v9
	v_mul_f32_e32 v0, 0xbfb8aa3b, v0
	v_mul_f32_e32 v1, 0xbfb8aa3b, v1
	v_mul_f32_e32 v8, 0xbfb8aa3b, v8
	v_mul_f32_e32 v9, 0xbfb8aa3b, v9
	v_exp_f32_e32 v0, v0
	v_exp_f32_e32 v1, v1
	v_add_f32_e32 v3, 1.0, v3
	v_exp_f32_e32 v8, v8
	v_exp_f32_e32 v9, v9
	v_add_f32_e32 v4, 1.0, v4
	v_rcp_f32_e32 v3, v3
	v_rcp_f32_e32 v10, v11
	v_rcp_f32_e32 v11, v4
	v_pk_add_f32 v[8:9], v[8:9], 1.0 op_sel_hi:[1,0]
	v_pk_add_f32 v[0:1], v[0:1], 1.0 op_sel_hi:[1,0]
	v_cvt_f32_fp8_e32 v4, v13
	v_pk_mul_f32 v[0:1], v[0:1], v[2:3]
	v_pk_mul_f32 v[2:3], v[8:9], v[10:11]
	v_pk_mul_f32 v[62:63], v[62:63], v[0:1]
	v_pk_mul_f32 v[64:65], v[64:65], v[2:3]
	v_cvt_f32_fp8_e32 v2, v5
	v_max_f32_e32 v0, v4, v4
	v_cvt_f32_fp8_sdwa v3, v13 src0_sel:BYTE_1
	v_cvt_f32_fp8_sdwa v4, v5 src0_sel:BYTE_1
	v_mul_f32_e32 v1, 0xbfb8aa3b, v2
	v_exp_f32_e32 v1, v1
	v_cvt_f32_fp8_sdwa v8, v5 src0_sel:BYTE_2
	v_cvt_f32_fp8_sdwa v5, v5 src0_sel:BYTE_3
	v_cvt_f32_fp8_sdwa v9, v13 src0_sel:BYTE_3
	v_add_f32_e32 v1, 1.0, v1
	v_rcp_f32_e32 v2, v1
	v_max_f32_e32 v1, v3, v3
	v_mul_f32_e32 v3, 0xbfb8aa3b, v4
	v_cvt_f32_fp8_sdwa v4, v13 src0_sel:BYTE_2
	v_mul_f32_e32 v8, 0xbfb8aa3b, v8
	v_mul_f32_e32 v5, 0xbfb8aa3b, v5
	v_exp_f32_e32 v3, v3
	v_exp_f32_e32 v8, v8
	v_exp_f32_e32 v10, v5
	v_max_f32_e32 v4, v4, v4
	v_max_f32_e32 v0, 0xc1f00000, v0
	v_max_f32_e32 v1, 0xc1f00000, v1
	v_max_f32_e32 v4, 0xc1f00000, v4
	v_max_f32_e32 v9, 0xc1f00000, v9
	v_mul_f32_e32 v0, 0xbfb8aa3b, v0
	v_mul_f32_e32 v1, 0xbfb8aa3b, v1
	v_mul_f32_e32 v4, 0xbfb8aa3b, v4
	v_mul_f32_e32 v5, 0xbfb8aa3b, v9
	v_exp_f32_e32 v0, v0
	v_exp_f32_e32 v1, v1
	v_add_f32_e32 v3, 1.0, v3
	v_exp_f32_e32 v4, v4
	v_add_f32_e32 v8, 1.0, v8
	v_exp_f32_e32 v5, v5
	v_add_f32_e32 v9, 1.0, v10
	v_rcp_f32_e32 v3, v3
	v_rcp_f32_e32 v8, v8
	v_rcp_f32_e32 v9, v9
	v_pk_add_f32 v[4:5], v[4:5], 1.0 op_sel_hi:[1,0]
	v_pk_add_f32 v[0:1], v[0:1], 1.0 op_sel_hi:[1,0]
	v_cvt_f32_fp8_sdwa v13, v14 src0_sel:BYTE_1
	v_pk_mul_f32 v[0:1], v[0:1], v[2:3]
	v_pk_mul_f32 v[2:3], v[4:5], v[8:9]
	v_cvt_f32_fp8_e32 v5, v6
	v_cvt_f32_fp8_e32 v4, v14
	v_pk_mul_f32 v[58:59], v[58:59], v[0:1]
	v_add_u32_e32 v8, 0xb0000, v16
	v_mul_f32_e32 v1, 0xbfb8aa3b, v5
	v_exp_f32_e32 v1, v1
	v_max_f32_e32 v0, v4, v4
	v_max_f32_e32 v0, 0xc1f00000, v0
	v_mul_f32_e32 v0, 0xbfb8aa3b, v0
	v_pk_mul_f32 v[60:61], v[60:61], v[2:3]
	v_exp_f32_e32 v4, v0
	v_add_f32_e32 v5, 1.0, v1
	global_load_dwordx4 v[0:3], v8, s[16:17]
	s_nop 0
	global_load_dwordx4 v[8:11], v8, s[16:17] offset:2048
	v_rcp_f32_e32 v12, v5
	v_max_f32_e32 v5, v13, v13
	v_mul_f32_e32 v13, 0xbfb8aa3b, v17
	v_cvt_f32_fp8_sdwa v17, v6 src0_sel:BYTE_2
	v_cvt_f32_fp8_sdwa v6, v6 src0_sel:BYTE_3
	v_cvt_f32_fp8_sdwa v16, v14 src0_sel:BYTE_2
	v_cvt_f32_fp8_sdwa v14, v14 src0_sel:BYTE_3
	v_mul_f32_e32 v17, 0xbfb8aa3b, v17
	v_mul_f32_e32 v6, 0xbfb8aa3b, v6
	v_exp_f32_e32 v13, v13
	v_exp_f32_e32 v17, v17
	v_exp_f32_e32 v6, v6
	v_max_f32_e32 v16, v16, v16
	v_max_f32_e32 v5, 0xc1f00000, v5
	v_max_f32_e32 v16, 0xc1f00000, v16
	v_max_f32_e32 v14, 0xc1f00000, v14
	v_mul_f32_e32 v5, 0xbfb8aa3b, v5
	v_mul_f32_e32 v16, 0xbfb8aa3b, v16
	v_mul_f32_e32 v14, 0xbfb8aa3b, v14
	v_exp_f32_e32 v5, v5
	v_add_f32_e32 v13, 1.0, v13
	v_exp_f32_e32 v16, v16
	v_add_f32_e32 v18, 1.0, v17
	v_exp_f32_e32 v17, v14
	v_add_f32_e32 v6, 1.0, v6
	v_rcp_f32_e32 v13, v13
	v_rcp_f32_e32 v18, v18
	v_rcp_f32_e32 v19, v6
	v_pk_add_f32 v[16:17], v[16:17], 1.0 op_sel_hi:[1,0]
	v_pk_add_f32 v[4:5], v[4:5], 1.0 op_sel_hi:[1,0]
	v_cvt_f32_fp8_e32 v6, v15
	v_pk_mul_f32 v[4:5], v[4:5], v[12:13]
	v_pk_mul_f32 v[12:13], v[16:17], v[18:19]
	v_pk_mul_f32 v[54:55], v[54:55], v[4:5]
	v_pk_mul_f32 v[56:57], v[56:57], v[12:13]
	v_cvt_f32_fp8_e32 v12, v7
	v_max_f32_e32 v4, v6, v6
	v_cvt_f32_fp8_sdwa v6, v15 src0_sel:BYTE_1
	v_cvt_f32_fp8_sdwa v13, v7 src0_sel:BYTE_1
	v_mul_f32_e32 v5, 0xbfb8aa3b, v12
	v_exp_f32_e32 v5, v5
	v_cvt_f32_fp8_sdwa v14, v15 src0_sel:BYTE_2
	v_cvt_f32_fp8_sdwa v15, v15 src0_sel:BYTE_3
	v_max_f32_e32 v4, 0xc1f00000, v4
	v_add_f32_e32 v5, 1.0, v5
	v_rcp_f32_e32 v12, v5
	v_max_f32_e32 v5, v6, v6
	v_mul_f32_e32 v6, 0xbfb8aa3b, v13
	v_exp_f32_e32 v6, v6
	v_max_f32_e32 v14, v14, v14
	v_max_f32_e32 v14, 0xc1f00000, v14
	v_mul_f32_e32 v14, 0xbfb8aa3b, v14
	v_add_f32_e32 v6, 1.0, v6
	v_rcp_f32_e32 v13, v6
	v_cvt_f32_fp8_sdwa v6, v7 src0_sel:BYTE_2
	v_cvt_f32_fp8_sdwa v7, v7 src0_sel:BYTE_3
	v_max_f32_e32 v15, 0xc1f00000, v15
	v_mul_f32_e32 v6, 0xbfb8aa3b, v6
	v_exp_f32_e32 v16, v6
	v_mul_f32_e32 v7, 0xbfb8aa3b, v7
	v_exp_f32_e32 v6, v14
	v_max_f32_e32 v5, 0xc1f00000, v5
	v_add_f32_e32 v14, 1.0, v16
	v_exp_f32_e32 v16, v7
	v_mul_f32_e32 v7, 0xbfb8aa3b, v15
	v_exp_f32_e32 v7, v7
	v_rcp_f32_e32 v14, v14
	v_add_f32_e32 v15, 1.0, v16
	v_rcp_f32_e32 v15, v15
	v_mul_f32_e32 v4, 0xbfb8aa3b, v4
	v_mul_f32_e32 v5, 0xbfb8aa3b, v5
	v_exp_f32_e32 v4, v4
	v_exp_f32_e32 v5, v5
	v_pk_add_f32 v[6:7], v[6:7], 1.0 op_sel_hi:[1,0]
	s_nop 7
	v_pk_add_f32 v[4:5], v[4:5], 1.0 op_sel_hi:[1,0]
	v_pk_mul_f32 v[6:7], v[6:7], v[14:15]
	v_pk_mul_f32 v[4:5], v[4:5], v[12:13]
	v_pk_mul_f32 v[52:53], v[52:53], v[6:7]
	s_waitcnt vmcnt(0)
	v_cvt_f32_fp8_e32 v6, v0
	v_cvt_f32_fp8_e32 v12, v8
	v_pk_mul_f32 v[50:51], v[50:51], v[4:5]
	v_cvt_f32_fp8_sdwa v7, v8 src0_sel:BYTE_1
	v_mul_f32_e32 v5, 0xbfb8aa3b, v6
	v_exp_f32_e32 v5, v5
	v_max_f32_e32 v4, v12, v12
	v_cvt_f32_fp8_sdwa v12, v0 src0_sel:BYTE_1
	v_cvt_f32_fp8_sdwa v13, v0 src0_sel:BYTE_2
	v_cvt_f32_fp8_sdwa v0, v0 src0_sel:BYTE_3
	v_add_f32_e32 v5, 1.0, v5
	v_rcp_f32_e32 v6, v5
	v_max_f32_e32 v5, v7, v7
	v_mul_f32_e32 v7, 0xbfb8aa3b, v12
	v_cvt_f32_fp8_sdwa v12, v8 src0_sel:BYTE_2
	v_cvt_f32_fp8_sdwa v8, v8 src0_sel:BYTE_3
	v_mul_f32_e32 v13, 0xbfb8aa3b, v13
	v_mul_f32_e32 v0, 0xbfb8aa3b, v0
	v_exp_f32_e32 v7, v7
	v_exp_f32_e32 v13, v13
	v_exp_f32_e32 v0, v0
	v_max_f32_e32 v12, v12, v12
	v_max_f32_e32 v4, 0xc1f00000, v4
	v_max_f32_e32 v5, 0xc1f00000, v5
	v_max_f32_e32 v12, 0xc1f00000, v12
	v_max_f32_e32 v8, 0xc1f00000, v8
	v_mul_f32_e32 v4, 0xbfb8aa3b, v4
	v_mul_f32_e32 v5, 0xbfb8aa3b, v5
	v_mul_f32_e32 v12, 0xbfb8aa3b, v12
	v_mul_f32_e32 v8, 0xbfb8aa3b, v8
	v_exp_f32_e32 v4, v4
	v_exp_f32_e32 v5, v5
	v_add_f32_e32 v7, 1.0, v7
	v_exp_f32_e32 v12, v12
	v_add_f32_e32 v14, 1.0, v13
	v_exp_f32_e32 v13, v8
	v_add_f32_e32 v0, 1.0, v0
	v_rcp_f32_e32 v7, v7
	v_rcp_f32_e32 v14, v14
	v_rcp_f32_e32 v15, v0
	v_pk_add_f32 v[12:13], v[12:13], 1.0 op_sel_hi:[1,0]
	v_pk_add_f32 v[4:5], v[4:5], 1.0 op_sel_hi:[1,0]
	v_cvt_f32_fp8_e32 v0, v9
	v_pk_mul_f32 v[4:5], v[4:5], v[6:7]
	v_pk_mul_f32 v[6:7], v[12:13], v[14:15]
	v_pk_mul_f32 v[46:47], v[46:47], v[4:5]
	v_pk_mul_f32 v[48:49], v[48:49], v[6:7]
	v_cvt_f32_fp8_e32 v6, v1
	v_max_f32_e32 v0, 0xc1f00000, v0
	v_mul_f32_e32 v0, 0xbfb8aa3b, v0
	v_mul_f32_e32 v4, 0xbfb8aa3b, v6
	v_exp_f32_e32 v5, v4
	v_exp_f32_e32 v4, v0
	v_cvt_f32_fp8_sdwa v0, v9 src0_sel:BYTE_1
	v_cvt_f32_fp8_sdwa v7, v1 src0_sel:BYTE_1
	v_add_f32_e32 v5, 1.0, v5
	v_cvt_f32_fp8_sdwa v8, v1 src0_sel:BYTE_2
	v_max_f32_e32 v0, 0xc1f00000, v0
	v_cvt_f32_fp8_sdwa v1, v1 src0_sel:BYTE_3
	v_rcp_f32_e32 v6, v5
	v_mul_f32_e32 v5, 0xbfb8aa3b, v7
	v_mul_f32_e32 v0, 0xbfb8aa3b, v0
	v_exp_f32_e32 v7, v5
	v_exp_f32_e32 v5, v0
	v_cvt_f32_fp8_sdwa v0, v9 src0_sel:BYTE_2
	v_cvt_f32_fp8_sdwa v9, v9 src0_sel:BYTE_3
	v_mul_f32_e32 v8, 0xbfb8aa3b, v8
	v_mul_f32_e32 v1, 0xbfb8aa3b, v1
	v_exp_f32_e32 v8, v8
	v_exp_f32_e32 v12, v1
	v_max_f32_e32 v0, v0, v0
	v_max_f32_e32 v0, 0xc1f00000, v0
	v_max_f32_e32 v9, 0xc1f00000, v9
	v_mul_f32_e32 v0, 0xbfb8aa3b, v0
	v_mul_f32_e32 v1, 0xbfb8aa3b, v9
	v_add_f32_e32 v7, 1.0, v7
	v_exp_f32_e32 v0, v0
	v_add_f32_e32 v8, 1.0, v8
	v_exp_f32_e32 v1, v1
	v_add_f32_e32 v9, 1.0, v12
	v_rcp_f32_e32 v7, v7
	v_rcp_f32_e32 v8, v8
	v_rcp_f32_e32 v9, v9
	v_pk_add_f32 v[0:1], v[0:1], 1.0 op_sel_hi:[1,0]
	v_pk_add_f32 v[4:5], v[4:5], 1.0 op_sel_hi:[1,0]
	v_pk_mul_f32 v[0:1], v[0:1], v[8:9]
	v_pk_mul_f32 v[4:5], v[4:5], v[6:7]
	v_cvt_f32_fp8_e32 v6, v10
	v_pk_mul_f32 v[44:45], v[44:45], v[0:1]
	v_cvt_f32_fp8_e32 v0, v2
	v_cvt_f32_fp8_sdwa v7, v2 src0_sel:BYTE_2
	v_pk_mul_f32 v[42:43], v[42:43], v[4:5]
	v_max_f32_e32 v1, v6, v6
	v_cvt_f32_fp8_sdwa v5, v2 src0_sel:BYTE_1
	v_cvt_f32_fp8_sdwa v2, v2 src0_sel:BYTE_3
	v_max_f32_e32 v1, 0xc1f00000, v1
	v_mul_f32_e32 v0, 0xbfb8aa3b, v0
	v_mul_f32_e32 v7, 0xbfb8aa3b, v7
	v_exp_f32_e32 v4, v0
	v_mul_f32_e32 v0, 0xbfb8aa3b, v1
	v_cvt_f32_fp8_sdwa v1, v10 src0_sel:BYTE_1
	v_cvt_f32_fp8_sdwa v6, v10 src0_sel:BYTE_2
	v_exp_f32_e32 v7, v7
	v_cvt_f32_fp8_sdwa v8, v10 src0_sel:BYTE_3
	v_mul_f32_e32 v5, 0xbfb8aa3b, v5
	v_mul_f32_e32 v2, 0xbfb8aa3b, v2
	v_exp_f32_e32 v5, v5
	v_exp_f32_e32 v2, v2
	v_max_f32_e32 v1, v1, v1
	v_add_f32_e32 v9, 1.0, v7
	v_max_f32_e32 v7, v8, v8
	v_max_f32_e32 v1, 0xc1f00000, v1
	v_max_f32_e32 v6, 0xc1f00000, v6
	v_max_f32_e32 v7, 0xc1f00000, v7
	v_mul_f32_e32 v1, 0xbfb8aa3b, v1
	v_mul_f32_e32 v6, 0xbfb8aa3b, v6
	v_mul_f32_e32 v7, 0xbfb8aa3b, v7
	v_exp_f32_e32 v0, v0
	v_add_f32_e32 v4, 1.0, v4
	v_exp_f32_e32 v1, v1
	v_add_f32_e32 v5, 1.0, v5
	v_exp_f32_e32 v6, v6
	v_exp_f32_e32 v7, v7
	v_add_f32_e32 v2, 1.0, v2
	v_rcp_f32_e32 v4, v4
	v_rcp_f32_e32 v5, v5
	v_rcp_f32_e32 v8, v9
	v_rcp_f32_e32 v9, v2
	v_pk_add_f32 v[6:7], v[6:7], 1.0 op_sel_hi:[1,0]
	v_pk_add_f32 v[0:1], v[0:1], 1.0 op_sel_hi:[1,0]
	v_cvt_f32_fp8_e32 v2, v11
	v_pk_mul_f32 v[0:1], v[0:1], v[4:5]
	v_pk_mul_f32 v[4:5], v[6:7], v[8:9]
	v_pk_mul_f32 v[38:39], v[38:39], v[0:1]
	v_pk_mul_f32 v[40:41], v[40:41], v[4:5]
	v_cvt_f32_fp8_e32 v4, v3
	v_max_f32_e32 v0, v2, v2
	v_cvt_f32_fp8_sdwa v2, v11 src0_sel:BYTE_1
	v_cvt_f32_fp8_sdwa v5, v3 src0_sel:BYTE_1
	v_mul_f32_e32 v1, 0xbfb8aa3b, v4
	v_exp_f32_e32 v1, v1
	v_cvt_f32_fp8_sdwa v6, v11 src0_sel:BYTE_2
	v_cvt_f32_fp8_sdwa v8, v11 src0_sel:BYTE_3
	v_max_f32_e32 v0, 0xc1f00000, v0
	v_add_f32_e32 v1, 1.0, v1
	v_rcp_f32_e32 v4, v1
	v_max_f32_e32 v1, v2, v2
	v_mul_f32_e32 v2, 0xbfb8aa3b, v5
	v_exp_f32_e32 v2, v2
	v_max_f32_e32 v6, v6, v6
	v_max_f32_e32 v6, 0xc1f00000, v6
	v_mul_f32_e32 v6, 0xbfb8aa3b, v6
	v_add_f32_e32 v2, 1.0, v2
	v_rcp_f32_e32 v5, v2
	v_cvt_f32_fp8_sdwa v2, v3 src0_sel:BYTE_2
	v_cvt_f32_fp8_sdwa v3, v3 src0_sel:BYTE_3
	v_max_f32_e32 v1, 0xc1f00000, v1
	v_mul_f32_e32 v0, 0xbfb8aa3b, v0
	v_mul_f32_e32 v2, 0xbfb8aa3b, v2
	v_exp_f32_e32 v7, v2
	v_mul_f32_e32 v3, 0xbfb8aa3b, v3
	v_exp_f32_e32 v2, v6
	v_mul_f32_e32 v1, 0xbfb8aa3b, v1
	v_add_f32_e32 v6, 1.0, v7
	v_max_f32_e32 v7, v8, v8
	v_exp_f32_e32 v8, v3
	v_max_f32_e32 v7, 0xc1f00000, v7
	v_mul_f32_e32 v3, 0xbfb8aa3b, v7
	v_exp_f32_e32 v0, v0
	v_exp_f32_e32 v1, v1
	v_exp_f32_e32 v3, v3
	v_add_f32_e32 v7, 1.0, v8
	v_rcp_f32_e32 v6, v6
	v_rcp_f32_e32 v7, v7
	v_pk_add_f32 v[2:3], v[2:3], 1.0 op_sel_hi:[1,0]
	v_pk_add_f32 v[0:1], v[0:1], 1.0 op_sel_hi:[1,0]
	v_pk_mul_f32 v[2:3], v[2:3], v[6:7]
	v_pk_mul_f32 v[0:1], v[0:1], v[4:5]
	v_pk_mul_f32 v[36:37], v[36:37], v[2:3]
	v_pk_mul_f32 v[34:35], v[34:35], v[0:1]
	s_cbranch_vccnz .LBB0_813
	s_barrier
	s_branch .LBB0_813

.LBB0_821:
	s_lshl_b32 s0, s0, 19
	v_add3_u32 v11, s0, v192, v199
	v_mov_b32_e32 v4, v33
	v_and_b32_e32 v8, 0x7ff, v11
	v_lshrrev_b32_e32 v9, 11, v11
	v_or_b32_e32 v10, 0x800, v8
	v_lshl_or_b32 v0, v9, 12, v10
	global_load_dwordx4 v[0:3], v0, s[16:17]
	v_mov_b32_e32 v5, v33
	s_and_b64 vcc, exec, s[4:5]
	s_mov_b64 s[4:5], -1
	s_waitcnt vmcnt(0)
	v_cvt_f32_fp8_e32 v6, v0
	v_cvt_f32_fp8_sdwa v7, v0 src0_sel:BYTE_1
	v_cvt_f32_fp8_e32 v13, v1
	v_cvt_f32_fp8_sdwa v14, v1 src0_sel:BYTE_1
	v_cvt_f32_fp8_sdwa v15, v1 src0_sel:BYTE_2
	v_cvt_f32_fp8_sdwa v1, v1 src0_sel:BYTE_3
	v_max_f32_e32 v6, 0xc1f00000, v6
	v_max_f32_e32 v7, 0xc1f00000, v7
	v_max_f32_e32 v13, 0xc1f00000, v13
	v_max_f32_e32 v14, 0xc1f00000, v14
	v_mul_f32_e32 v6, 0xbfb8aa3b, v6
	v_mul_f32_e32 v7, 0xbfb8aa3b, v7
	v_cvt_f32_fp8_sdwa v12, v0 src0_sel:BYTE_2
	v_cvt_f32_fp8_sdwa v0, v0 src0_sel:BYTE_3
	v_mul_f32_e32 v13, 0xbfb8aa3b, v13
	v_mul_f32_e32 v14, 0xbfb8aa3b, v14
	v_exp_f32_e32 v6, v6
	v_exp_f32_e32 v7, v7
	v_cvt_f32_fp8_e32 v16, v2
	v_cvt_f32_fp8_sdwa v17, v2 src0_sel:BYTE_1
	v_exp_f32_e32 v13, v13
	v_exp_f32_e32 v14, v14
	v_max_f32_e32 v15, v15, v15
	v_max_f32_e32 v1, v1, v1
	v_max_f32_e32 v15, 0xc1f00000, v15
	v_max_f32_e32 v1, 0xc1f00000, v1
	v_mul_f32_e32 v15, 0xbfb8aa3b, v15
	v_mul_f32_e32 v1, 0xbfb8aa3b, v1
	v_add_f32_e32 v6, 1.0, v6
	v_add_f32_e32 v7, 1.0, v7
	v_cvt_f32_fp8_sdwa v18, v2 src0_sel:BYTE_2
	v_cvt_f32_fp8_sdwa v2, v2 src0_sel:BYTE_3
	v_max_f32_e32 v16, v16, v16
	v_max_f32_e32 v17, v17, v17
	v_max_f32_e32 v12, 0xc1f00000, v12
	v_max_f32_e32 v0, 0xc1f00000, v0
	v_exp_f32_e32 v15, v15
	v_exp_f32_e32 v1, v1
	v_add_f32_e32 v13, 1.0, v13
	v_add_f32_e32 v14, 1.0, v14
	v_rcp_f32_e32 v6, v6
	v_rcp_f32_e32 v7, v7
	v_max_f32_e32 v16, 0xc1f00000, v16
	v_max_f32_e32 v17, 0xc1f00000, v17
	v_mul_f32_e32 v12, 0xbfb8aa3b, v12
	v_mul_f32_e32 v0, 0xbfb8aa3b, v0
	v_rcp_f32_e32 v13, v13
	v_rcp_f32_e32 v14, v14
	v_mul_f32_e32 v16, 0xbfb8aa3b, v16
	v_mul_f32_e32 v17, 0xbfb8aa3b, v17
	v_exp_f32_e32 v12, v12
	v_exp_f32_e32 v0, v0
	v_exp_f32_e32 v16, v16
	v_exp_f32_e32 v17, v17
	v_max_f32_e32 v18, v18, v18
	v_add_f32_e32 v15, 1.0, v15
	v_add_f32_e32 v1, 1.0, v1
	v_mul_f32_e32 v6, v158, v6
	v_mul_f32_e32 v7, v159, v7
	v_max_f32_e32 v2, v2, v2
	v_max_f32_e32 v18, 0xc1f00000, v18
	v_rcp_f32_e32 v15, v15
	v_rcp_f32_e32 v1, v1
	v_mul_f32_e32 v13, v154, v13
	v_mul_f32_e32 v14, v155, v14
	v_mul_f32_e32 v6, 0x41800000, v6
	v_mul_f32_e32 v7, 0x41800000, v7
	v_max_f32_e32 v2, 0xc1f00000, v2
	v_mul_f32_e32 v18, 0xbfb8aa3b, v18
	v_add_f32_e32 v12, 1.0, v12
	v_add_f32_e32 v0, 1.0, v0
	v_mul_f32_e32 v13, 0x41800000, v13
	v_mul_f32_e32 v14, 0x41800000, v14
	v_cvt_pk_fp8_f32 v4, v6, v7
	v_mul_f32_e32 v2, 0xbfb8aa3b, v2
	v_cvt_f32_fp8_e32 v6, v3
	v_exp_f32_e32 v18, v18
	v_add_f32_e32 v16, 1.0, v16
	v_add_f32_e32 v17, 1.0, v17
	v_rcp_f32_e32 v12, v12
	v_rcp_f32_e32 v0, v0
	v_cvt_pk_fp8_f32 v5, v13, v14
	v_exp_f32_e32 v2, v2
	v_rcp_f32_e32 v16, v16
	v_rcp_f32_e32 v17, v17
	v_mul_f32_e32 v15, v156, v15
	v_mul_f32_e32 v1, v157, v1
	v_mul_f32_e32 v15, 0x41800000, v15
	v_mul_f32_e32 v1, 0x41800000, v1
	v_mul_f32_e32 v12, v160, v12
	v_mul_f32_e32 v0, v161, v0
	v_cvt_pk_fp8_f32 v5, v15, v1 op_sel:[0,0,1]
	v_add_f32_e32 v1, 1.0, v18
	v_add_f32_e32 v2, 1.0, v2
	v_max_f32_e32 v6, 0xc1f00000, v6
	v_mul_f32_e32 v16, v150, v16
	v_mul_f32_e32 v17, v151, v17
	v_mul_f32_e32 v12, 0x41800000, v12
	v_mul_f32_e32 v0, 0x41800000, v0
	v_rcp_f32_e32 v1, v1
	v_rcp_f32_e32 v2, v2
	v_mul_f32_e32 v6, 0xbfb8aa3b, v6
	v_mul_f32_e32 v7, 0x41800000, v16
	v_cvt_pk_fp8_f32 v4, v12, v0 op_sel:[0,0,1]
	v_mul_f32_e32 v0, 0x41800000, v17
	v_exp_f32_e32 v12, v6
	v_mov_b32_e32 v6, v33
	v_cvt_pk_fp8_f32 v6, v7, v0
	v_cvt_f32_fp8_sdwa v7, v3 src0_sel:BYTE_1
	v_mul_f32_e32 v1, v152, v1
	v_mul_f32_e32 v2, v153, v2
	v_mul_f32_e32 v1, 0x41800000, v1
	v_mul_f32_e32 v2, 0x41800000, v2
	v_cvt_pk_fp8_f32 v6, v1, v2 op_sel:[0,0,1]
	v_max_f32_e32 v1, v7, v7
	v_cvt_f32_fp8_sdwa v2, v3 src0_sel:BYTE_2
	v_cvt_f32_fp8_sdwa v3, v3 src0_sel:BYTE_3
	v_max_f32_e32 v1, 0xc1f00000, v1
	v_mul_f32_e32 v1, 0xbfb8aa3b, v1
	v_exp_f32_e32 v1, v1
	v_max_f32_e32 v2, v2, v2
	v_max_f32_e32 v2, 0xc1f00000, v2
	v_max_f32_e32 v3, 0xc1f00000, v3
	v_mul_f32_e32 v2, 0xbfb8aa3b, v2
	v_mul_f32_e32 v3, 0xbfb8aa3b, v3
	v_add_f32_e32 v0, 1.0, v12
	v_exp_f32_e32 v2, v2
	v_add_f32_e32 v1, 1.0, v1
	v_exp_f32_e32 v3, v3
	v_rcp_f32_e32 v0, v0
	v_rcp_f32_e32 v1, v1
	v_add_f32_e32 v2, 1.0, v2
	v_add_f32_e32 v3, 1.0, v3
	v_mul_f32_e32 v0, v146, v0
	v_rcp_f32_e32 v2, v2
	v_mul_f32_e32 v1, v147, v1
	v_rcp_f32_e32 v3, v3
	v_mul_f32_e32 v0, 0x41800000, v0
	v_mul_f32_e32 v1, 0x41800000, v1
	v_mov_b32_e32 v7, v33
	v_cvt_pk_fp8_f32 v7, v0, v1
	v_mul_f32_e32 v2, v148, v2
	v_mul_f32_e32 v1, v149, v3
	v_mul_f32_e32 v0, 0x41800000, v2
	v_mul_f32_e32 v1, 0x41800000, v1
	v_cvt_pk_fp8_f32 v7, v0, v1 op_sel:[0,0,1]
	global_store_dwordx4 v11, v[4:7], s[14:15]
	v_add_u32_e32 v11, 16, v9
	v_lshl_or_b32 v0, v11, 12, v10
	global_load_dwordx4 v[0:3], v0, s[16:17]
	v_mov_b32_e32 v4, v33
	s_waitcnt vmcnt(0)
	v_cvt_f32_fp8_e32 v5, v0
	v_cvt_f32_fp8_sdwa v6, v0 src0_sel:BYTE_1
	v_cvt_f32_fp8_sdwa v7, v0 src0_sel:BYTE_2
	v_cvt_f32_fp8_sdwa v0, v0 src0_sel:BYTE_3
	v_max_f32_e32 v5, 0xc1f00000, v5
	v_max_f32_e32 v6, 0xc1f00000, v6
	v_mul_f32_e32 v5, 0xbfb8aa3b, v5
	v_mul_f32_e32 v6, 0xbfb8aa3b, v6
	v_exp_f32_e32 v5, v5
	v_exp_f32_e32 v6, v6
	v_max_f32_e32 v7, v7, v7
	v_add_f32_e32 v5, 1.0, v5
	v_add_f32_e32 v6, 1.0, v6
	v_rcp_f32_e32 v5, v5
	v_rcp_f32_e32 v6, v6
	v_max_f32_e32 v7, 0xc1f00000, v7
	v_max_f32_e32 v0, 0xc1f00000, v0
	v_mul_f32_e32 v5, v142, v5
	v_mul_f32_e32 v6, v143, v6
	v_cvt_f32_fp8_sdwa v13, v1 src0_sel:BYTE_1
	v_mul_f32_e32 v7, 0xbfb8aa3b, v7
	v_mul_f32_e32 v0, 0xbfb8aa3b, v0
	v_mul_f32_e32 v5, 0x41800000, v5
	v_mul_f32_e32 v6, 0x41800000, v6
	v_cvt_f32_fp8_e32 v12, v1
	v_exp_f32_e32 v7, v7
	v_exp_f32_e32 v0, v0
	v_cvt_pk_fp8_f32 v4, v5, v6
	v_cvt_f32_fp8_sdwa v6, v1 src0_sel:BYTE_2
	v_max_f32_e32 v5, v13, v13
	v_add_f32_e32 v7, 1.0, v7
	v_add_f32_e32 v0, 1.0, v0
	v_max_f32_e32 v5, 0xc1f00000, v5
	v_cvt_f32_fp8_sdwa v1, v1 src0_sel:BYTE_3
	v_max_f32_e32 v12, 0xc1f00000, v12
	v_rcp_f32_e32 v7, v7
	v_rcp_f32_e32 v0, v0
	v_mul_f32_e32 v5, 0xbfb8aa3b, v5
	v_max_f32_e32 v6, 0xc1f00000, v6
	v_mul_f32_e32 v12, 0xbfb8aa3b, v12
	v_exp_f32_e32 v5, v5
	v_mul_f32_e32 v6, 0xbfb8aa3b, v6
	v_exp_f32_e32 v12, v12
	v_exp_f32_e32 v6, v6
	v_max_f32_e32 v1, v1, v1
	v_mul_f32_e32 v7, v144, v7
	v_mul_f32_e32 v0, v145, v0
	v_max_f32_e32 v1, 0xc1f00000, v1
	v_mul_f32_e32 v7, 0x41800000, v7
	v_mul_f32_e32 v0, 0x41800000, v0
	v_add_f32_e32 v5, 1.0, v5
	v_mul_f32_e32 v1, 0xbfb8aa3b, v1
	v_cvt_pk_fp8_f32 v4, v7, v0 op_sel:[0,0,1]
	v_add_f32_e32 v0, 1.0, v12
	v_rcp_f32_e32 v5, v5
	v_exp_f32_e32 v1, v1
	v_add_f32_e32 v6, 1.0, v6
	v_rcp_f32_e32 v0, v0
	v_rcp_f32_e32 v6, v6
	v_mul_f32_e32 v5, v139, v5
	v_add_f32_e32 v1, 1.0, v1
	v_mul_f32_e32 v0, v138, v0
	v_mul_f32_e32 v7, 0x41800000, v5
	v_rcp_f32_e32 v1, v1
	v_mul_f32_e32 v5, v140, v6
	v_mul_f32_e32 v0, 0x41800000, v0
	v_mul_f32_e32 v6, 0x41800000, v5
	v_mov_b32_e32 v5, v33
	v_cvt_pk_fp8_f32 v5, v0, v7
	v_mul_f32_e32 v1, v141, v1
	v_mul_f32_e32 v1, 0x41800000, v1
	v_cvt_f32_fp8_e32 v12, v2
	v_cvt_pk_fp8_f32 v5, v6, v1 op_sel:[0,0,1]
	v_cvt_f32_fp8_sdwa v6, v2 src0_sel:BYTE_2
	v_cvt_f32_fp8_sdwa v7, v2 src0_sel:BYTE_1
	v_cvt_f32_fp8_sdwa v2, v2 src0_sel:BYTE_3
	v_max_f32_e32 v0, v12, v12
	v_max_f32_e32 v6, 0xc1f00000, v6
	v_mul_f32_e32 v6, 0xbfb8aa3b, v6
	v_max_f32_e32 v1, v7, v7
	v_exp_f32_e32 v6, v6
	v_max_f32_e32 v0, 0xc1f00000, v0
	v_max_f32_e32 v1, 0xc1f00000, v1
	v_mul_f32_e32 v0, 0xbfb8aa3b, v0
	v_mul_f32_e32 v1, 0xbfb8aa3b, v1
	v_max_f32_e32 v2, 0xc1f00000, v2
	v_exp_f32_e32 v0, v0
	v_exp_f32_e32 v1, v1
	v_mul_f32_e32 v2, 0xbfb8aa3b, v2
	v_add_f32_e32 v6, 1.0, v6
	v_exp_f32_e32 v2, v2
	v_rcp_f32_e32 v6, v6
	v_cvt_f32_fp8_e32 v7, v3
	v_add_f32_e32 v0, 1.0, v0
	v_add_f32_e32 v1, 1.0, v1
	v_rcp_f32_e32 v0, v0
	v_rcp_f32_e32 v1, v1
	v_add_f32_e32 v2, 1.0, v2
	v_mul_f32_e32 v6, v136, v6
	v_rcp_f32_e32 v2, v2
	v_mul_f32_e32 v12, 0x41800000, v6
	v_max_f32_e32 v6, v7, v7
	v_max_f32_e32 v6, 0xc1f00000, v6
	v_mul_f32_e32 v0, v134, v0
	v_mul_f32_e32 v1, v135, v1
	v_mul_f32_e32 v6, 0xbfb8aa3b, v6
	v_mul_f32_e32 v0, 0x41800000, v0
	v_mul_f32_e32 v1, 0x41800000, v1
	v_exp_f32_e32 v7, v6
	v_mul_f32_e32 v2, v137, v2
	v_mov_b32_e32 v6, v33
	v_cvt_pk_fp8_f32 v6, v0, v1
	v_mul_f32_e32 v1, 0x41800000, v2
	v_cvt_f32_fp8_sdwa v2, v3 src0_sel:BYTE_1
	v_add_f32_e32 v0, 1.0, v7
	v_cvt_pk_fp8_f32 v6, v12, v1 op_sel:[0,0,1]
	v_rcp_f32_e32 v0, v0
	v_max_f32_e32 v1, v2, v2
	v_cvt_f32_fp8_sdwa v2, v3 src0_sel:BYTE_2
	v_cvt_f32_fp8_sdwa v3, v3 src0_sel:BYTE_3
	v_max_f32_e32 v1, 0xc1f00000, v1
	v_mul_f32_e32 v1, 0xbfb8aa3b, v1
	v_exp_f32_e32 v1, v1
	v_max_f32_e32 v2, v2, v2
	v_max_f32_e32 v2, 0xc1f00000, v2
	v_max_f32_e32 v3, 0xc1f00000, v3
	v_mul_f32_e32 v2, 0xbfb8aa3b, v2
	v_mul_f32_e32 v3, 0xbfb8aa3b, v3
	v_exp_f32_e32 v2, v2
	v_add_f32_e32 v1, 1.0, v1
	v_exp_f32_e32 v3, v3
	v_rcp_f32_e32 v1, v1
	v_add_f32_e32 v2, 1.0, v2
	v_mul_f32_e32 v0, v130, v0
	v_add_f32_e32 v3, 1.0, v3
	v_rcp_f32_e32 v2, v2
	v_mul_f32_e32 v1, v131, v1
	v_rcp_f32_e32 v3, v3
	v_mul_f32_e32 v0, 0x41800000, v0
	v_mul_f32_e32 v1, 0x41800000, v1
	v_mov_b32_e32 v7, v33
	v_cvt_pk_fp8_f32 v7, v0, v1
	v_mul_f32_e32 v2, v132, v2
	v_mul_f32_e32 v1, v133, v3
	v_mul_f32_e32 v0, 0x41800000, v2
	v_mul_f32_e32 v1, 0x41800000, v1
	v_cvt_pk_fp8_f32 v7, v0, v1 op_sel:[0,0,1]
	v_lshl_or_b32 v0, v11, 11, v8
	global_store_dwordx4 v0, v[4:7], s[14:15]
	s_nop 1
	v_add_u32_e32 v4, 32, v9
	v_lshl_or_b32 v0, v4, 12, v10
	global_load_dwordx4 v[0:3], v0, s[16:17]
	v_lshl_or_b32 v4, v4, 11, v8
	s_waitcnt vmcnt(0)
	v_cvt_f32_fp8_e32 v5, v0
	v_cvt_f32_fp8_sdwa v6, v0 src0_sel:BYTE_1
	v_cvt_f32_fp8_sdwa v7, v0 src0_sel:BYTE_2
	v_cvt_f32_fp8_sdwa v0, v0 src0_sel:BYTE_3
	v_max_f32_e32 v5, 0xc1f00000, v5
	v_max_f32_e32 v6, 0xc1f00000, v6
	v_max_f32_e32 v0, 0xc1f00000, v0
	v_mul_f32_e32 v5, 0xbfb8aa3b, v5
	v_mul_f32_e32 v6, 0xbfb8aa3b, v6
	v_mul_f32_e32 v0, 0xbfb8aa3b, v0
	v_exp_f32_e32 v5, v5
	v_exp_f32_e32 v6, v6
	v_exp_f32_e32 v0, v0
	v_max_f32_e32 v7, v7, v7
	v_max_f32_e32 v7, 0xc1f00000, v7
	v_mul_f32_e32 v7, 0xbfb8aa3b, v7
	v_add_f32_e32 v5, 1.0, v5
	v_add_f32_e32 v6, 1.0, v6
	v_exp_f32_e32 v7, v7
	v_add_f32_e32 v0, 1.0, v0
	v_rcp_f32_e32 v5, v5
	v_rcp_f32_e32 v6, v6
	v_rcp_f32_e32 v0, v0
	v_add_f32_e32 v7, 1.0, v7
	v_mul_f32_e32 v5, v126, v5
	v_mul_f32_e32 v6, v127, v6
	v_rcp_f32_e32 v7, v7
	v_mul_f32_e32 v0, v129, v0
	v_mul_f32_e32 v5, 0x41800000, v5
	v_mul_f32_e32 v6, 0x41800000, v6
	v_mul_f32_e32 v12, 0x41800000, v0
	v_mov_b32_e32 v0, v33
	v_cvt_pk_fp8_f32 v0, v5, v6
	v_mul_f32_e32 v7, v128, v7
	v_mul_f32_e32 v7, 0x41800000, v7
	v_cvt_f32_fp8_e32 v11, v1
	v_cvt_f32_fp8_sdwa v6, v1 src0_sel:BYTE_1
	v_cvt_pk_fp8_f32 v0, v7, v12 op_sel:[0,0,1]
	v_cvt_f32_fp8_sdwa v7, v1 src0_sel:BYTE_2
	v_cvt_f32_fp8_sdwa v1, v1 src0_sel:BYTE_3
	v_max_f32_e32 v5, v11, v11
	v_max_f32_e32 v5, 0xc1f00000, v5
	v_max_f32_e32 v6, 0xc1f00000, v6
	v_mul_f32_e32 v5, 0xbfb8aa3b, v5
	v_mul_f32_e32 v6, 0xbfb8aa3b, v6
	v_max_f32_e32 v1, 0xc1f00000, v1
	v_exp_f32_e32 v5, v5
	v_exp_f32_e32 v6, v6
	v_mul_f32_e32 v1, 0xbfb8aa3b, v1
	v_exp_f32_e32 v1, v1
	v_max_f32_e32 v7, 0xc1f00000, v7
	v_mul_f32_e32 v7, 0xbfb8aa3b, v7
	v_add_f32_e32 v5, 1.0, v5
	v_add_f32_e32 v6, 1.0, v6
	v_exp_f32_e32 v7, v7
	v_rcp_f32_e32 v5, v5
	v_rcp_f32_e32 v6, v6
	v_add_f32_e32 v1, 1.0, v1
	v_rcp_f32_e32 v1, v1
	v_add_f32_e32 v7, 1.0, v7
	v_mul_f32_e32 v5, v122, v5
	v_mul_f32_e32 v6, v123, v6
	v_rcp_f32_e32 v7, v7
	v_mul_f32_e32 v5, 0x41800000, v5
	v_mul_f32_e32 v6, 0x41800000, v6
	v_cvt_f32_fp8_e32 v11, v2
	v_mul_f32_e32 v12, v125, v1
	v_mov_b32_e32 v1, v33
	v_cvt_pk_fp8_f32 v1, v5, v6
	v_mul_f32_e32 v7, v124, v7
	v_mul_f32_e32 v7, 0x41800000, v7
	v_max_f32_e32 v5, v11, v11
	v_mul_f32_e32 v6, 0x41800000, v12
	v_cvt_f32_fp8_sdwa v11, v2 src0_sel:BYTE_1
	v_cvt_pk_fp8_f32 v1, v7, v6 op_sel:[0,0,1]
	v_cvt_f32_fp8_sdwa v7, v2 src0_sel:BYTE_2
	v_cvt_f32_fp8_sdwa v2, v2 src0_sel:BYTE_3
	v_max_f32_e32 v6, v11, v11
	v_max_f32_e32 v5, 0xc1f00000, v5
	v_max_f32_e32 v6, 0xc1f00000, v6
	v_mul_f32_e32 v5, 0xbfb8aa3b, v5
	v_mul_f32_e32 v6, 0xbfb8aa3b, v6
	v_max_f32_e32 v2, 0xc1f00000, v2
	v_exp_f32_e32 v5, v5
	v_exp_f32_e32 v6, v6
	v_mul_f32_e32 v2, 0xbfb8aa3b, v2
	v_cvt_f32_fp8_e32 v11, v3
	v_exp_f32_e32 v2, v2
	v_max_f32_e32 v7, 0xc1f00000, v7
	v_mul_f32_e32 v7, 0xbfb8aa3b, v7
	v_add_f32_e32 v5, 1.0, v5
	v_add_f32_e32 v6, 1.0, v6
	v_exp_f32_e32 v7, v7
	v_max_f32_e32 v11, v11, v11
	v_rcp_f32_e32 v5, v5
	v_rcp_f32_e32 v6, v6
	v_add_f32_e32 v2, 1.0, v2
	v_max_f32_e32 v11, 0xc1f00000, v11
	v_rcp_f32_e32 v2, v2
	v_mul_f32_e32 v11, 0xbfb8aa3b, v11
	v_exp_f32_e32 v11, v11
	v_add_f32_e32 v7, 1.0, v7
	v_mul_f32_e32 v5, v118, v5
	v_mul_f32_e32 v6, v119, v6
	v_rcp_f32_e32 v7, v7
	v_mul_f32_e32 v5, 0x41800000, v5
	v_mul_f32_e32 v6, 0x41800000, v6
	v_mul_f32_e32 v12, v121, v2
	v_mov_b32_e32 v2, v33
	v_cvt_pk_fp8_f32 v2, v5, v6
	v_add_f32_e32 v5, 1.0, v11
	v_cvt_f32_fp8_sdwa v11, v3 src0_sel:BYTE_1
	v_mul_f32_e32 v7, v120, v7
	v_mul_f32_e32 v7, 0x41800000, v7
	v_mul_f32_e32 v6, 0x41800000, v12
	v_cvt_pk_fp8_f32 v2, v7, v6 op_sel:[0,0,1]
	v_max_f32_e32 v6, v11, v11
	v_cvt_f32_fp8_sdwa v7, v3 src0_sel:BYTE_2
	v_cvt_f32_fp8_sdwa v3, v3 src0_sel:BYTE_3
	v_max_f32_e32 v6, 0xc1f00000, v6
	v_mul_f32_e32 v6, 0xbfb8aa3b, v6
	v_exp_f32_e32 v6, v6
	v_max_f32_e32 v7, v7, v7
	v_max_f32_e32 v7, 0xc1f00000, v7
	v_max_f32_e32 v3, 0xc1f00000, v3
	v_mul_f32_e32 v7, 0xbfb8aa3b, v7
	v_mul_f32_e32 v3, 0xbfb8aa3b, v3
	v_exp_f32_e32 v7, v7
	v_add_f32_e32 v6, 1.0, v6
	v_exp_f32_e32 v3, v3
	v_rcp_f32_e32 v5, v5
	v_rcp_f32_e32 v6, v6
	v_add_f32_e32 v7, 1.0, v7
	v_add_f32_e32 v3, 1.0, v3
	v_mul_f32_e32 v5, v114, v5
	v_rcp_f32_e32 v7, v7
	v_mul_f32_e32 v6, v115, v6
	v_rcp_f32_e32 v11, v3
	v_mul_f32_e32 v5, 0x41800000, v5
	v_mul_f32_e32 v6, 0x41800000, v6
	v_mov_b32_e32 v3, v33
	v_cvt_pk_fp8_f32 v3, v5, v6
	v_mul_f32_e32 v7, v116, v7
	v_mul_f32_e32 v6, v117, v11
	v_mul_f32_e32 v5, 0x41800000, v7
	v_mul_f32_e32 v6, 0x41800000, v6
	v_cvt_pk_fp8_f32 v3, v5, v6 op_sel:[0,0,1]
	global_store_dwordx4 v4, v[0:3], s[14:15]
	v_add_u32_e32 v4, 48, v9
	s_nop 0
	v_lshl_or_b32 v0, v4, 12, v10
	global_load_dwordx4 v[0:3], v0, s[16:17]
	v_lshl_or_b32 v4, v4, 11, v8
	s_waitcnt vmcnt(0)
	v_cvt_f32_fp8_e32 v5, v0
	v_cvt_f32_fp8_sdwa v6, v0 src0_sel:BYTE_1
	v_cvt_f32_fp8_sdwa v7, v0 src0_sel:BYTE_2
	v_cvt_f32_fp8_sdwa v0, v0 src0_sel:BYTE_3
	v_max_f32_e32 v5, 0xc1f00000, v5
	v_max_f32_e32 v6, 0xc1f00000, v6
	v_max_f32_e32 v0, 0xc1f00000, v0
	v_mul_f32_e32 v5, 0xbfb8aa3b, v5
	v_mul_f32_e32 v6, 0xbfb8aa3b, v6
	v_mul_f32_e32 v0, 0xbfb8aa3b, v0
	v_exp_f32_e32 v5, v5
	v_exp_f32_e32 v6, v6
	v_exp_f32_e32 v0, v0
	v_max_f32_e32 v7, v7, v7
	v_max_f32_e32 v7, 0xc1f00000, v7
	v_mul_f32_e32 v7, 0xbfb8aa3b, v7
	v_add_f32_e32 v5, 1.0, v5
	v_add_f32_e32 v6, 1.0, v6
	v_exp_f32_e32 v7, v7
	v_add_f32_e32 v0, 1.0, v0
	v_rcp_f32_e32 v5, v5
	v_rcp_f32_e32 v6, v6
	v_rcp_f32_e32 v0, v0
	v_add_f32_e32 v7, 1.0, v7
	v_mul_f32_e32 v5, v110, v5
	v_mul_f32_e32 v6, v111, v6
	v_rcp_f32_e32 v7, v7
	v_mul_f32_e32 v0, v113, v0
	v_mul_f32_e32 v5, 0x41800000, v5
	v_mul_f32_e32 v6, 0x41800000, v6
	v_mul_f32_e32 v12, 0x41800000, v0
	v_mov_b32_e32 v0, v33
	v_cvt_pk_fp8_f32 v0, v5, v6
	v_mul_f32_e32 v7, v112, v7
	v_mul_f32_e32 v7, 0x41800000, v7
	v_cvt_f32_fp8_e32 v11, v1
	v_cvt_f32_fp8_sdwa v6, v1 src0_sel:BYTE_1
	v_cvt_pk_fp8_f32 v0, v7, v12 op_sel:[0,0,1]
	v_cvt_f32_fp8_sdwa v7, v1 src0_sel:BYTE_2
	v_cvt_f32_fp8_sdwa v1, v1 src0_sel:BYTE_3
	v_max_f32_e32 v5, v11, v11
	v_max_f32_e32 v5, 0xc1f00000, v5
	v_max_f32_e32 v6, 0xc1f00000, v6
	v_mul_f32_e32 v5, 0xbfb8aa3b, v5
	v_mul_f32_e32 v6, 0xbfb8aa3b, v6
	v_max_f32_e32 v1, 0xc1f00000, v1
	v_exp_f32_e32 v5, v5
	v_exp_f32_e32 v6, v6
	v_mul_f32_e32 v1, 0xbfb8aa3b, v1
	v_exp_f32_e32 v1, v1
	v_max_f32_e32 v7, 0xc1f00000, v7
	v_mul_f32_e32 v7, 0xbfb8aa3b, v7
	v_add_f32_e32 v5, 1.0, v5
	v_add_f32_e32 v6, 1.0, v6
	v_exp_f32_e32 v7, v7
	v_rcp_f32_e32 v5, v5
	v_rcp_f32_e32 v6, v6
	v_add_f32_e32 v1, 1.0, v1
	v_rcp_f32_e32 v1, v1
	v_add_f32_e32 v7, 1.0, v7
	v_mul_f32_e32 v5, v106, v5
	v_mul_f32_e32 v6, v107, v6
	v_rcp_f32_e32 v7, v7
	v_mul_f32_e32 v5, 0x41800000, v5
	v_mul_f32_e32 v6, 0x41800000, v6
	v_cvt_f32_fp8_e32 v11, v2
	v_mul_f32_e32 v12, v109, v1
	v_mov_b32_e32 v1, v33
	v_cvt_pk_fp8_f32 v1, v5, v6
	v_mul_f32_e32 v7, v108, v7
	v_mul_f32_e32 v7, 0x41800000, v7
	v_max_f32_e32 v5, v11, v11
	v_mul_f32_e32 v6, 0x41800000, v12
	v_cvt_f32_fp8_sdwa v11, v2 src0_sel:BYTE_1
	v_cvt_pk_fp8_f32 v1, v7, v6 op_sel:[0,0,1]
	v_cvt_f32_fp8_sdwa v7, v2 src0_sel:BYTE_2
	v_cvt_f32_fp8_sdwa v2, v2 src0_sel:BYTE_3
	v_max_f32_e32 v6, v11, v11
	v_max_f32_e32 v5, 0xc1f00000, v5
	v_max_f32_e32 v6, 0xc1f00000, v6
	v_mul_f32_e32 v5, 0xbfb8aa3b, v5
	v_mul_f32_e32 v6, 0xbfb8aa3b, v6
	v_max_f32_e32 v2, 0xc1f00000, v2
	v_exp_f32_e32 v5, v5
	v_exp_f32_e32 v6, v6
	v_mul_f32_e32 v2, 0xbfb8aa3b, v2
	v_cvt_f32_fp8_e32 v11, v3
	v_exp_f32_e32 v2, v2
	v_max_f32_e32 v7, 0xc1f00000, v7
	v_mul_f32_e32 v7, 0xbfb8aa3b, v7
	v_add_f32_e32 v5, 1.0, v5
	v_add_f32_e32 v6, 1.0, v6
	v_exp_f32_e32 v7, v7
	v_max_f32_e32 v11, v11, v11
	v_rcp_f32_e32 v5, v5
	v_rcp_f32_e32 v6, v6
	v_add_f32_e32 v2, 1.0, v2
	v_max_f32_e32 v11, 0xc1f00000, v11
	v_rcp_f32_e32 v2, v2
	v_mul_f32_e32 v11, 0xbfb8aa3b, v11
	v_exp_f32_e32 v11, v11
	v_add_f32_e32 v7, 1.0, v7
	v_mul_f32_e32 v5, v102, v5
	v_mul_f32_e32 v6, v103, v6
	v_rcp_f32_e32 v7, v7
	v_mul_f32_e32 v5, 0x41800000, v5
	v_mul_f32_e32 v6, 0x41800000, v6
	v_mul_f32_e32 v12, v105, v2
	v_mov_b32_e32 v2, v33
	v_cvt_pk_fp8_f32 v2, v5, v6
	v_add_f32_e32 v5, 1.0, v11
	v_cvt_f32_fp8_sdwa v11, v3 src0_sel:BYTE_1
	v_mul_f32_e32 v7, v104, v7
	v_mul_f32_e32 v7, 0x41800000, v7
	v_mul_f32_e32 v6, 0x41800000, v12
	v_cvt_pk_fp8_f32 v2, v7, v6 op_sel:[0,0,1]
	v_max_f32_e32 v6, v11, v11
	v_cvt_f32_fp8_sdwa v7, v3 src0_sel:BYTE_2
	v_cvt_f32_fp8_sdwa v3, v3 src0_sel:BYTE_3
	v_max_f32_e32 v6, 0xc1f00000, v6
	v_mul_f32_e32 v6, 0xbfb8aa3b, v6
	v_exp_f32_e32 v6, v6
	v_max_f32_e32 v7, v7, v7
	v_max_f32_e32 v7, 0xc1f00000, v7
	v_max_f32_e32 v3, 0xc1f00000, v3
	v_mul_f32_e32 v7, 0xbfb8aa3b, v7
	v_mul_f32_e32 v3, 0xbfb8aa3b, v3
	v_exp_f32_e32 v7, v7
	v_add_f32_e32 v6, 1.0, v6
	v_exp_f32_e32 v3, v3
	v_rcp_f32_e32 v5, v5
	v_rcp_f32_e32 v6, v6
	v_add_f32_e32 v7, 1.0, v7
	v_add_f32_e32 v3, 1.0, v3
	v_mul_f32_e32 v5, v98, v5
	v_rcp_f32_e32 v7, v7
	v_mul_f32_e32 v6, v99, v6
	v_rcp_f32_e32 v11, v3
	v_mul_f32_e32 v5, 0x41800000, v5
	v_mul_f32_e32 v6, 0x41800000, v6
	v_mov_b32_e32 v3, v33
	v_cvt_pk_fp8_f32 v3, v5, v6
	v_mul_f32_e32 v7, v100, v7
	v_mul_f32_e32 v6, v101, v11
	v_mul_f32_e32 v5, 0x41800000, v7
	v_mul_f32_e32 v6, 0x41800000, v6
	v_cvt_pk_fp8_f32 v3, v5, v6 op_sel:[0,0,1]
	global_store_dwordx4 v4, v[0:3], s[14:15]
	v_add_u32_e32 v4, 0x80, v9
	s_nop 0
	v_lshl_or_b32 v0, v4, 12, v10
	global_load_dwordx4 v[0:3], v0, s[16:17]
	v_lshl_or_b32 v4, v4, 11, v8
	s_waitcnt vmcnt(0)
	v_cvt_f32_fp8_e32 v5, v0
	v_cvt_f32_fp8_sdwa v6, v0 src0_sel:BYTE_1
	v_cvt_f32_fp8_sdwa v7, v0 src0_sel:BYTE_2
	v_cvt_f32_fp8_sdwa v0, v0 src0_sel:BYTE_3
	v_max_f32_e32 v5, 0xc1f00000, v5
	v_max_f32_e32 v6, 0xc1f00000, v6
	v_max_f32_e32 v0, 0xc1f00000, v0
	v_mul_f32_e32 v5, 0xbfb8aa3b, v5
	v_mul_f32_e32 v6, 0xbfb8aa3b, v6
	v_mul_f32_e32 v0, 0xbfb8aa3b, v0
	v_exp_f32_e32 v5, v5
	v_exp_f32_e32 v6, v6
	v_exp_f32_e32 v0, v0
	v_max_f32_e32 v7, v7, v7
	v_max_f32_e32 v7, 0xc1f00000, v7
	v_mul_f32_e32 v7, 0xbfb8aa3b, v7
	v_add_f32_e32 v5, 1.0, v5
	v_add_f32_e32 v6, 1.0, v6
	v_exp_f32_e32 v7, v7
	v_add_f32_e32 v0, 1.0, v0
	v_rcp_f32_e32 v5, v5
	v_rcp_f32_e32 v6, v6
	v_rcp_f32_e32 v0, v0
	v_add_f32_e32 v7, 1.0, v7
	v_mul_f32_e32 v5, v94, v5
	v_mul_f32_e32 v6, v95, v6
	v_rcp_f32_e32 v7, v7
	v_mul_f32_e32 v0, v97, v0
	v_mul_f32_e32 v5, 0x41800000, v5
	v_mul_f32_e32 v6, 0x41800000, v6
	v_mul_f32_e32 v12, 0x41800000, v0
	v_mov_b32_e32 v0, v33
	v_cvt_pk_fp8_f32 v0, v5, v6
	v_mul_f32_e32 v7, v96, v7
	v_mul_f32_e32 v7, 0x41800000, v7
	v_cvt_f32_fp8_e32 v11, v1
	v_cvt_f32_fp8_sdwa v6, v1 src0_sel:BYTE_1
	v_cvt_pk_fp8_f32 v0, v7, v12 op_sel:[0,0,1]
	v_cvt_f32_fp8_sdwa v7, v1 src0_sel:BYTE_2
	v_cvt_f32_fp8_sdwa v1, v1 src0_sel:BYTE_3
	v_max_f32_e32 v5, v11, v11
	v_max_f32_e32 v5, 0xc1f00000, v5
	v_max_f32_e32 v6, 0xc1f00000, v6
	v_mul_f32_e32 v5, 0xbfb8aa3b, v5
	v_mul_f32_e32 v6, 0xbfb8aa3b, v6
	v_max_f32_e32 v1, 0xc1f00000, v1
	v_exp_f32_e32 v5, v5
	v_exp_f32_e32 v6, v6
	v_mul_f32_e32 v1, 0xbfb8aa3b, v1
	v_exp_f32_e32 v1, v1
	v_max_f32_e32 v7, 0xc1f00000, v7
	v_mul_f32_e32 v7, 0xbfb8aa3b, v7
	v_add_f32_e32 v5, 1.0, v5
	v_add_f32_e32 v6, 1.0, v6
	v_exp_f32_e32 v7, v7
	v_rcp_f32_e32 v5, v5
	v_rcp_f32_e32 v6, v6
	v_add_f32_e32 v1, 1.0, v1
	v_rcp_f32_e32 v1, v1
	v_add_f32_e32 v7, 1.0, v7
	v_mul_f32_e32 v5, v90, v5
	v_mul_f32_e32 v6, v91, v6
	v_rcp_f32_e32 v7, v7
	v_mul_f32_e32 v5, 0x41800000, v5
	v_mul_f32_e32 v6, 0x41800000, v6
	v_cvt_f32_fp8_e32 v11, v2
	v_mul_f32_e32 v12, v93, v1
	v_mov_b32_e32 v1, v33
	v_cvt_pk_fp8_f32 v1, v5, v6
	v_mul_f32_e32 v7, v92, v7
	v_mul_f32_e32 v7, 0x41800000, v7
	v_max_f32_e32 v5, v11, v11
	v_mul_f32_e32 v6, 0x41800000, v12
	v_cvt_f32_fp8_sdwa v11, v2 src0_sel:BYTE_1
	v_cvt_pk_fp8_f32 v1, v7, v6 op_sel:[0,0,1]
	v_cvt_f32_fp8_sdwa v7, v2 src0_sel:BYTE_2
	v_cvt_f32_fp8_sdwa v2, v2 src0_sel:BYTE_3
	v_max_f32_e32 v6, v11, v11
	v_max_f32_e32 v5, 0xc1f00000, v5
	v_max_f32_e32 v6, 0xc1f00000, v6
	v_mul_f32_e32 v5, 0xbfb8aa3b, v5
	v_mul_f32_e32 v6, 0xbfb8aa3b, v6
	v_max_f32_e32 v2, 0xc1f00000, v2
	v_exp_f32_e32 v5, v5
	v_exp_f32_e32 v6, v6
	v_mul_f32_e32 v2, 0xbfb8aa3b, v2
	v_cvt_f32_fp8_e32 v11, v3
	v_exp_f32_e32 v2, v2
	v_max_f32_e32 v7, 0xc1f00000, v7
	v_mul_f32_e32 v7, 0xbfb8aa3b, v7
	v_add_f32_e32 v5, 1.0, v5
	v_add_f32_e32 v6, 1.0, v6
	v_exp_f32_e32 v7, v7
	v_max_f32_e32 v11, v11, v11
	v_rcp_f32_e32 v5, v5
	v_rcp_f32_e32 v6, v6
	v_add_f32_e32 v2, 1.0, v2
	v_max_f32_e32 v11, 0xc1f00000, v11
	v_rcp_f32_e32 v2, v2
	v_mul_f32_e32 v11, 0xbfb8aa3b, v11
	v_exp_f32_e32 v11, v11
	v_add_f32_e32 v7, 1.0, v7
	v_mul_f32_e32 v5, v86, v5
	v_mul_f32_e32 v6, v87, v6
	v_rcp_f32_e32 v7, v7
	v_mul_f32_e32 v5, 0x41800000, v5
	v_mul_f32_e32 v6, 0x41800000, v6
	v_mul_f32_e32 v12, v89, v2
	v_mov_b32_e32 v2, v33
	v_cvt_pk_fp8_f32 v2, v5, v6
	v_add_f32_e32 v5, 1.0, v11
	v_cvt_f32_fp8_sdwa v11, v3 src0_sel:BYTE_1
	v_mul_f32_e32 v7, v88, v7
	v_mul_f32_e32 v7, 0x41800000, v7
	v_mul_f32_e32 v6, 0x41800000, v12
	v_cvt_pk_fp8_f32 v2, v7, v6 op_sel:[0,0,1]
	v_max_f32_e32 v6, v11, v11
	v_cvt_f32_fp8_sdwa v7, v3 src0_sel:BYTE_2
	v_cvt_f32_fp8_sdwa v3, v3 src0_sel:BYTE_3
	v_max_f32_e32 v6, 0xc1f00000, v6
	v_mul_f32_e32 v6, 0xbfb8aa3b, v6
	v_exp_f32_e32 v6, v6
	v_max_f32_e32 v7, v7, v7
	v_max_f32_e32 v7, 0xc1f00000, v7
	v_max_f32_e32 v3, 0xc1f00000, v3
	v_mul_f32_e32 v7, 0xbfb8aa3b, v7
	v_mul_f32_e32 v3, 0xbfb8aa3b, v3
	v_exp_f32_e32 v7, v7
	v_add_f32_e32 v6, 1.0, v6
	v_exp_f32_e32 v3, v3
	v_rcp_f32_e32 v5, v5
	v_rcp_f32_e32 v6, v6
	v_add_f32_e32 v7, 1.0, v7
	v_add_f32_e32 v3, 1.0, v3
	v_mul_f32_e32 v5, v82, v5
	v_rcp_f32_e32 v7, v7
	v_mul_f32_e32 v6, v83, v6
	v_rcp_f32_e32 v11, v3
	v_mul_f32_e32 v5, 0x41800000, v5
	v_mul_f32_e32 v6, 0x41800000, v6
	v_mov_b32_e32 v3, v33
	v_cvt_pk_fp8_f32 v3, v5, v6
	v_mul_f32_e32 v7, v84, v7
	v_mul_f32_e32 v6, v85, v11
	v_mul_f32_e32 v5, 0x41800000, v7
	v_mul_f32_e32 v6, 0x41800000, v6
	v_cvt_pk_fp8_f32 v3, v5, v6 op_sel:[0,0,1]
	global_store_dwordx4 v4, v[0:3], s[14:15]
	v_add_u32_e32 v4, 0x90, v9
	s_nop 0
	v_lshl_or_b32 v0, v4, 12, v10
	global_load_dwordx4 v[0:3], v0, s[16:17]
	v_lshl_or_b32 v4, v4, 11, v8
	s_waitcnt vmcnt(0)
	v_cvt_f32_fp8_e32 v5, v0
	v_cvt_f32_fp8_sdwa v6, v0 src0_sel:BYTE_1
	v_cvt_f32_fp8_sdwa v7, v0 src0_sel:BYTE_2
	v_cvt_f32_fp8_sdwa v0, v0 src0_sel:BYTE_3
	v_max_f32_e32 v5, 0xc1f00000, v5
	v_max_f32_e32 v6, 0xc1f00000, v6
	v_max_f32_e32 v0, 0xc1f00000, v0
	v_mul_f32_e32 v5, 0xbfb8aa3b, v5
	v_mul_f32_e32 v6, 0xbfb8aa3b, v6
	v_mul_f32_e32 v0, 0xbfb8aa3b, v0
	v_exp_f32_e32 v5, v5
	v_exp_f32_e32 v6, v6
	v_exp_f32_e32 v0, v0
	v_max_f32_e32 v7, v7, v7
	v_max_f32_e32 v7, 0xc1f00000, v7
	v_mul_f32_e32 v7, 0xbfb8aa3b, v7
	v_add_f32_e32 v5, 1.0, v5
	v_add_f32_e32 v6, 1.0, v6
	v_exp_f32_e32 v7, v7
	v_add_f32_e32 v0, 1.0, v0
	v_rcp_f32_e32 v5, v5
	v_rcp_f32_e32 v6, v6
	v_rcp_f32_e32 v0, v0
	v_add_f32_e32 v7, 1.0, v7
	v_mul_f32_e32 v5, v78, v5
	v_mul_f32_e32 v6, v79, v6
	v_rcp_f32_e32 v7, v7
	v_mul_f32_e32 v0, v81, v0
	v_mul_f32_e32 v5, 0x41800000, v5
	v_mul_f32_e32 v6, 0x41800000, v6
	v_mul_f32_e32 v12, 0x41800000, v0
	v_mov_b32_e32 v0, v33
	v_cvt_pk_fp8_f32 v0, v5, v6
	v_mul_f32_e32 v7, v80, v7
	v_mul_f32_e32 v7, 0x41800000, v7
	v_cvt_f32_fp8_e32 v11, v1
	v_cvt_f32_fp8_sdwa v6, v1 src0_sel:BYTE_1
	v_cvt_pk_fp8_f32 v0, v7, v12 op_sel:[0,0,1]
	v_cvt_f32_fp8_sdwa v7, v1 src0_sel:BYTE_2
	v_cvt_f32_fp8_sdwa v1, v1 src0_sel:BYTE_3
	v_max_f32_e32 v5, v11, v11
	v_max_f32_e32 v5, 0xc1f00000, v5
	v_max_f32_e32 v6, 0xc1f00000, v6
	v_mul_f32_e32 v5, 0xbfb8aa3b, v5
	v_mul_f32_e32 v6, 0xbfb8aa3b, v6
	v_max_f32_e32 v1, 0xc1f00000, v1
	v_exp_f32_e32 v5, v5
	v_exp_f32_e32 v6, v6
	v_mul_f32_e32 v1, 0xbfb8aa3b, v1
	v_exp_f32_e32 v1, v1
	v_max_f32_e32 v7, 0xc1f00000, v7
	v_mul_f32_e32 v7, 0xbfb8aa3b, v7
	v_add_f32_e32 v5, 1.0, v5
	v_add_f32_e32 v6, 1.0, v6
	v_exp_f32_e32 v7, v7
	v_rcp_f32_e32 v5, v5
	v_rcp_f32_e32 v6, v6
	v_add_f32_e32 v1, 1.0, v1
	v_rcp_f32_e32 v1, v1
	v_add_f32_e32 v7, 1.0, v7
	v_mul_f32_e32 v5, v74, v5
	v_mul_f32_e32 v6, v75, v6
	v_rcp_f32_e32 v7, v7
	v_mul_f32_e32 v5, 0x41800000, v5
	v_mul_f32_e32 v6, 0x41800000, v6
	v_cvt_f32_fp8_e32 v11, v2
	v_mul_f32_e32 v12, v77, v1
	v_mov_b32_e32 v1, v33
	v_cvt_pk_fp8_f32 v1, v5, v6
	v_mul_f32_e32 v7, v76, v7
	v_mul_f32_e32 v7, 0x41800000, v7
	v_max_f32_e32 v5, v11, v11
	v_mul_f32_e32 v6, 0x41800000, v12
	v_cvt_f32_fp8_sdwa v11, v2 src0_sel:BYTE_1
	v_cvt_pk_fp8_f32 v1, v7, v6 op_sel:[0,0,1]
	v_cvt_f32_fp8_sdwa v7, v2 src0_sel:BYTE_2
	v_cvt_f32_fp8_sdwa v2, v2 src0_sel:BYTE_3
	v_max_f32_e32 v6, v11, v11
	v_max_f32_e32 v5, 0xc1f00000, v5
	v_max_f32_e32 v6, 0xc1f00000, v6
	v_mul_f32_e32 v5, 0xbfb8aa3b, v5
	v_mul_f32_e32 v6, 0xbfb8aa3b, v6
	v_max_f32_e32 v2, 0xc1f00000, v2
	v_exp_f32_e32 v5, v5
	v_exp_f32_e32 v6, v6
	v_mul_f32_e32 v2, 0xbfb8aa3b, v2
	v_cvt_f32_fp8_e32 v11, v3
	v_exp_f32_e32 v2, v2
	v_max_f32_e32 v7, 0xc1f00000, v7
	v_mul_f32_e32 v7, 0xbfb8aa3b, v7
	v_add_f32_e32 v5, 1.0, v5
	v_add_f32_e32 v6, 1.0, v6
	v_exp_f32_e32 v7, v7
	v_max_f32_e32 v11, v11, v11
	v_rcp_f32_e32 v5, v5
	v_rcp_f32_e32 v6, v6
	v_add_f32_e32 v2, 1.0, v2
	v_max_f32_e32 v11, 0xc1f00000, v11
	v_rcp_f32_e32 v2, v2
	v_mul_f32_e32 v11, 0xbfb8aa3b, v11
	v_exp_f32_e32 v11, v11
	v_add_f32_e32 v7, 1.0, v7
	v_mul_f32_e32 v5, v70, v5
	v_mul_f32_e32 v6, v71, v6
	v_rcp_f32_e32 v7, v7
	v_mul_f32_e32 v5, 0x41800000, v5
	v_mul_f32_e32 v6, 0x41800000, v6
	v_mul_f32_e32 v12, v73, v2
	v_mov_b32_e32 v2, v33
	v_cvt_pk_fp8_f32 v2, v5, v6
	v_add_f32_e32 v5, 1.0, v11
	v_cvt_f32_fp8_sdwa v11, v3 src0_sel:BYTE_1
	v_mul_f32_e32 v7, v72, v7
	v_mul_f32_e32 v7, 0x41800000, v7
	v_mul_f32_e32 v6, 0x41800000, v12
	v_cvt_pk_fp8_f32 v2, v7, v6 op_sel:[0,0,1]
	v_max_f32_e32 v6, v11, v11
	v_cvt_f32_fp8_sdwa v7, v3 src0_sel:BYTE_2
	v_cvt_f32_fp8_sdwa v3, v3 src0_sel:BYTE_3
	v_max_f32_e32 v6, 0xc1f00000, v6
	v_mul_f32_e32 v6, 0xbfb8aa3b, v6
	v_exp_f32_e32 v6, v6
	v_max_f32_e32 v7, v7, v7
	v_max_f32_e32 v7, 0xc1f00000, v7
	v_max_f32_e32 v3, 0xc1f00000, v3
	v_mul_f32_e32 v7, 0xbfb8aa3b, v7
	v_mul_f32_e32 v3, 0xbfb8aa3b, v3
	v_exp_f32_e32 v7, v7
	v_add_f32_e32 v6, 1.0, v6
	v_exp_f32_e32 v3, v3
	v_rcp_f32_e32 v5, v5
	v_rcp_f32_e32 v6, v6
	v_add_f32_e32 v7, 1.0, v7
	v_add_f32_e32 v3, 1.0, v3
	v_mul_f32_e32 v5, v66, v5
	v_rcp_f32_e32 v7, v7
	v_mul_f32_e32 v6, v67, v6
	v_rcp_f32_e32 v11, v3
	v_mul_f32_e32 v5, 0x41800000, v5
	v_mul_f32_e32 v6, 0x41800000, v6
	v_mov_b32_e32 v3, v33
	v_cvt_pk_fp8_f32 v3, v5, v6
	v_mul_f32_e32 v7, v68, v7
	v_mul_f32_e32 v6, v69, v11
	v_mul_f32_e32 v5, 0x41800000, v7
	v_mul_f32_e32 v6, 0x41800000, v6
	v_cvt_pk_fp8_f32 v3, v5, v6 op_sel:[0,0,1]
	global_store_dwordx4 v4, v[0:3], s[14:15]
	v_add_u32_e32 v4, 0xa0, v9
	s_nop 0
	v_lshl_or_b32 v0, v4, 12, v10
	global_load_dwordx4 v[0:3], v0, s[16:17]
	v_lshl_or_b32 v4, v4, 11, v8
	s_waitcnt vmcnt(0)
	v_cvt_f32_fp8_e32 v5, v0
	v_cvt_f32_fp8_sdwa v6, v0 src0_sel:BYTE_1
	v_cvt_f32_fp8_sdwa v7, v0 src0_sel:BYTE_2
	v_cvt_f32_fp8_sdwa v0, v0 src0_sel:BYTE_3
	v_max_f32_e32 v5, 0xc1f00000, v5
	v_max_f32_e32 v6, 0xc1f00000, v6
	v_max_f32_e32 v0, 0xc1f00000, v0
	v_mul_f32_e32 v5, 0xbfb8aa3b, v5
	v_mul_f32_e32 v6, 0xbfb8aa3b, v6
	v_mul_f32_e32 v0, 0xbfb8aa3b, v0
	v_exp_f32_e32 v5, v5
	v_exp_f32_e32 v6, v6
	v_exp_f32_e32 v0, v0
	v_max_f32_e32 v7, v7, v7
	v_max_f32_e32 v7, 0xc1f00000, v7
	v_mul_f32_e32 v7, 0xbfb8aa3b, v7
	v_add_f32_e32 v5, 1.0, v5
	v_add_f32_e32 v6, 1.0, v6
	v_exp_f32_e32 v7, v7
	v_add_f32_e32 v0, 1.0, v0
	v_rcp_f32_e32 v5, v5
	v_rcp_f32_e32 v6, v6
	v_rcp_f32_e32 v0, v0
	v_add_f32_e32 v7, 1.0, v7
	v_mul_f32_e32 v5, v62, v5
	v_mul_f32_e32 v6, v63, v6
	v_rcp_f32_e32 v7, v7
	v_mul_f32_e32 v0, v65, v0
	v_mul_f32_e32 v5, 0x41800000, v5
	v_mul_f32_e32 v6, 0x41800000, v6
	v_mul_f32_e32 v12, 0x41800000, v0
	v_mov_b32_e32 v0, v33
	v_cvt_pk_fp8_f32 v0, v5, v6
	v_mul_f32_e32 v7, v64, v7
	v_mul_f32_e32 v7, 0x41800000, v7
	v_cvt_f32_fp8_e32 v11, v1
	v_cvt_f32_fp8_sdwa v6, v1 src0_sel:BYTE_1
	v_cvt_pk_fp8_f32 v0, v7, v12 op_sel:[0,0,1]
	v_cvt_f32_fp8_sdwa v7, v1 src0_sel:BYTE_2
	v_cvt_f32_fp8_sdwa v1, v1 src0_sel:BYTE_3
	v_max_f32_e32 v5, v11, v11
	v_max_f32_e32 v5, 0xc1f00000, v5
	v_max_f32_e32 v6, 0xc1f00000, v6
	v_mul_f32_e32 v5, 0xbfb8aa3b, v5
	v_mul_f32_e32 v6, 0xbfb8aa3b, v6
	v_max_f32_e32 v1, 0xc1f00000, v1
	v_exp_f32_e32 v5, v5
	v_exp_f32_e32 v6, v6
	v_mul_f32_e32 v1, 0xbfb8aa3b, v1
	v_exp_f32_e32 v1, v1
	v_max_f32_e32 v7, 0xc1f00000, v7
	v_mul_f32_e32 v7, 0xbfb8aa3b, v7
	v_add_f32_e32 v5, 1.0, v5
	v_add_f32_e32 v6, 1.0, v6
	v_exp_f32_e32 v7, v7
	v_rcp_f32_e32 v5, v5
	v_rcp_f32_e32 v6, v6
	v_add_f32_e32 v1, 1.0, v1
	v_rcp_f32_e32 v1, v1
	v_add_f32_e32 v7, 1.0, v7
	v_mul_f32_e32 v5, v58, v5
	v_mul_f32_e32 v6, v59, v6
	v_rcp_f32_e32 v7, v7
	v_mul_f32_e32 v5, 0x41800000, v5
	v_mul_f32_e32 v6, 0x41800000, v6
	v_cvt_f32_fp8_e32 v11, v2
	v_mul_f32_e32 v12, v61, v1
	v_mov_b32_e32 v1, v33
	v_cvt_pk_fp8_f32 v1, v5, v6
	v_mul_f32_e32 v7, v60, v7
	v_mul_f32_e32 v7, 0x41800000, v7
	v_max_f32_e32 v5, v11, v11
	v_mul_f32_e32 v6, 0x41800000, v12
	v_cvt_f32_fp8_sdwa v11, v2 src0_sel:BYTE_1
	v_cvt_pk_fp8_f32 v1, v7, v6 op_sel:[0,0,1]
	v_cvt_f32_fp8_sdwa v7, v2 src0_sel:BYTE_2
	v_cvt_f32_fp8_sdwa v2, v2 src0_sel:BYTE_3
	v_max_f32_e32 v6, v11, v11
	v_max_f32_e32 v5, 0xc1f00000, v5
	v_max_f32_e32 v6, 0xc1f00000, v6
	v_mul_f32_e32 v5, 0xbfb8aa3b, v5
	v_mul_f32_e32 v6, 0xbfb8aa3b, v6
	v_max_f32_e32 v2, 0xc1f00000, v2
	v_exp_f32_e32 v5, v5
	v_exp_f32_e32 v6, v6
	v_mul_f32_e32 v2, 0xbfb8aa3b, v2
	v_cvt_f32_fp8_e32 v11, v3
	v_exp_f32_e32 v2, v2
	v_max_f32_e32 v7, 0xc1f00000, v7
	v_mul_f32_e32 v7, 0xbfb8aa3b, v7
	v_add_f32_e32 v5, 1.0, v5
	v_add_f32_e32 v6, 1.0, v6
	v_exp_f32_e32 v7, v7
	v_max_f32_e32 v11, v11, v11
	v_rcp_f32_e32 v5, v5
	v_rcp_f32_e32 v6, v6
	v_add_f32_e32 v2, 1.0, v2
	v_max_f32_e32 v11, 0xc1f00000, v11
	v_rcp_f32_e32 v2, v2
	v_mul_f32_e32 v11, 0xbfb8aa3b, v11
	v_exp_f32_e32 v11, v11
	v_add_f32_e32 v7, 1.0, v7
	v_mul_f32_e32 v5, v54, v5
	v_mul_f32_e32 v6, v55, v6
	v_rcp_f32_e32 v7, v7
	v_mul_f32_e32 v5, 0x41800000, v5
	v_mul_f32_e32 v6, 0x41800000, v6
	v_mul_f32_e32 v12, v57, v2
	v_mov_b32_e32 v2, v33
	v_cvt_pk_fp8_f32 v2, v5, v6
	v_add_f32_e32 v5, 1.0, v11
	v_cvt_f32_fp8_sdwa v11, v3 src0_sel:BYTE_1
	v_mul_f32_e32 v7, v56, v7
	v_mul_f32_e32 v7, 0x41800000, v7
	v_mul_f32_e32 v6, 0x41800000, v12
	v_cvt_pk_fp8_f32 v2, v7, v6 op_sel:[0,0,1]
	v_max_f32_e32 v6, v11, v11
	v_cvt_f32_fp8_sdwa v7, v3 src0_sel:BYTE_2
	v_cvt_f32_fp8_sdwa v3, v3 src0_sel:BYTE_3
	v_max_f32_e32 v6, 0xc1f00000, v6
	v_mul_f32_e32 v6, 0xbfb8aa3b, v6
	v_exp_f32_e32 v6, v6
	v_max_f32_e32 v7, v7, v7
	v_max_f32_e32 v7, 0xc1f00000, v7
	v_max_f32_e32 v3, 0xc1f00000, v3
	v_mul_f32_e32 v7, 0xbfb8aa3b, v7
	v_mul_f32_e32 v3, 0xbfb8aa3b, v3
	v_exp_f32_e32 v7, v7
	v_add_f32_e32 v6, 1.0, v6
	v_exp_f32_e32 v3, v3
	v_rcp_f32_e32 v5, v5
	v_rcp_f32_e32 v6, v6
	v_add_f32_e32 v7, 1.0, v7
	v_add_f32_e32 v3, 1.0, v3
	v_mul_f32_e32 v5, v50, v5
	v_rcp_f32_e32 v7, v7
	v_mul_f32_e32 v6, v51, v6
	v_rcp_f32_e32 v11, v3
	v_mul_f32_e32 v5, 0x41800000, v5
	v_mul_f32_e32 v6, 0x41800000, v6
	v_mov_b32_e32 v3, v33
	v_cvt_pk_fp8_f32 v3, v5, v6
	v_mul_f32_e32 v7, v52, v7
	v_mul_f32_e32 v6, v53, v11
	v_mul_f32_e32 v5, 0x41800000, v7
	v_mul_f32_e32 v6, 0x41800000, v6
	v_cvt_pk_fp8_f32 v3, v5, v6 op_sel:[0,0,1]
	global_store_dwordx4 v4, v[0:3], s[14:15]
	v_add_u32_e32 v4, 0xb0, v9
	s_nop 0
	v_lshl_or_b32 v0, v4, 12, v10
	global_load_dwordx4 v[0:3], v0, s[16:17]
	v_lshl_or_b32 v4, v4, 11, v8
	s_waitcnt vmcnt(0)
	v_cvt_f32_fp8_e32 v5, v0
	v_cvt_f32_fp8_sdwa v6, v0 src0_sel:BYTE_1
	v_cvt_f32_fp8_sdwa v7, v0 src0_sel:BYTE_2
	v_cvt_f32_fp8_sdwa v0, v0 src0_sel:BYTE_3
	v_max_f32_e32 v5, 0xc1f00000, v5
	v_max_f32_e32 v6, 0xc1f00000, v6
	v_max_f32_e32 v0, 0xc1f00000, v0
	v_mul_f32_e32 v5, 0xbfb8aa3b, v5
	v_mul_f32_e32 v6, 0xbfb8aa3b, v6
	v_mul_f32_e32 v0, 0xbfb8aa3b, v0
	v_exp_f32_e32 v5, v5
	v_exp_f32_e32 v6, v6
	v_exp_f32_e32 v0, v0
	v_max_f32_e32 v7, v7, v7
	v_max_f32_e32 v7, 0xc1f00000, v7
	v_mul_f32_e32 v7, 0xbfb8aa3b, v7
	v_add_f32_e32 v5, 1.0, v5
	v_add_f32_e32 v6, 1.0, v6
	v_exp_f32_e32 v7, v7
	v_add_f32_e32 v0, 1.0, v0
	v_rcp_f32_e32 v5, v5
	v_rcp_f32_e32 v6, v6
	v_rcp_f32_e32 v0, v0
	v_add_f32_e32 v7, 1.0, v7
	v_mul_f32_e32 v5, v46, v5
	v_mul_f32_e32 v6, v47, v6
	v_rcp_f32_e32 v7, v7
	v_mul_f32_e32 v0, v49, v0
	v_mul_f32_e32 v5, 0x41800000, v5
	v_mul_f32_e32 v6, 0x41800000, v6
	v_mul_f32_e32 v10, 0x41800000, v0
	v_mov_b32_e32 v0, v33
	v_cvt_pk_fp8_f32 v0, v5, v6
	v_mul_f32_e32 v7, v48, v7
	v_mul_f32_e32 v7, 0x41800000, v7
	v_cvt_f32_fp8_e32 v9, v1
	v_cvt_f32_fp8_sdwa v6, v1 src0_sel:BYTE_1
	v_cvt_pk_fp8_f32 v0, v7, v10 op_sel:[0,0,1]
	v_cvt_f32_fp8_sdwa v7, v1 src0_sel:BYTE_2
	v_cvt_f32_fp8_sdwa v1, v1 src0_sel:BYTE_3
	v_max_f32_e32 v5, v9, v9
	v_max_f32_e32 v5, 0xc1f00000, v5
	v_max_f32_e32 v6, 0xc1f00000, v6
	v_mul_f32_e32 v5, 0xbfb8aa3b, v5
	v_mul_f32_e32 v6, 0xbfb8aa3b, v6
	v_max_f32_e32 v1, 0xc1f00000, v1
	v_exp_f32_e32 v5, v5
	v_exp_f32_e32 v6, v6
	v_mul_f32_e32 v1, 0xbfb8aa3b, v1
	v_exp_f32_e32 v1, v1
	v_max_f32_e32 v7, 0xc1f00000, v7
	v_mul_f32_e32 v7, 0xbfb8aa3b, v7
	v_add_f32_e32 v5, 1.0, v5
	v_add_f32_e32 v6, 1.0, v6
	v_exp_f32_e32 v7, v7
	v_rcp_f32_e32 v5, v5
	v_rcp_f32_e32 v6, v6
	v_add_f32_e32 v1, 1.0, v1
	v_rcp_f32_e32 v1, v1
	v_add_f32_e32 v7, 1.0, v7
	v_mul_f32_e32 v5, v42, v5
	v_mul_f32_e32 v6, v43, v6
	v_rcp_f32_e32 v7, v7
	v_mul_f32_e32 v5, 0x41800000, v5
	v_mul_f32_e32 v6, 0x41800000, v6
	v_cvt_f32_fp8_e32 v9, v2
	v_mul_f32_e32 v10, v45, v1
	v_mov_b32_e32 v1, v33
	v_cvt_pk_fp8_f32 v1, v5, v6
	v_mul_f32_e32 v7, v44, v7
	v_mul_f32_e32 v7, 0x41800000, v7
	v_max_f32_e32 v5, v9, v9
	v_mul_f32_e32 v6, 0x41800000, v10
	v_cvt_f32_fp8_sdwa v9, v2 src0_sel:BYTE_1
	v_cvt_pk_fp8_f32 v1, v7, v6 op_sel:[0,0,1]
	v_cvt_f32_fp8_sdwa v7, v2 src0_sel:BYTE_2
	v_cvt_f32_fp8_sdwa v2, v2 src0_sel:BYTE_3
	v_max_f32_e32 v6, v9, v9
	v_max_f32_e32 v5, 0xc1f00000, v5
	v_max_f32_e32 v6, 0xc1f00000, v6
	v_mul_f32_e32 v5, 0xbfb8aa3b, v5
	v_mul_f32_e32 v6, 0xbfb8aa3b, v6
	v_max_f32_e32 v2, 0xc1f00000, v2
	v_exp_f32_e32 v5, v5
	v_exp_f32_e32 v6, v6
	v_mul_f32_e32 v2, 0xbfb8aa3b, v2
	v_cvt_f32_fp8_e32 v9, v3
	v_exp_f32_e32 v2, v2
	v_max_f32_e32 v7, 0xc1f00000, v7
	v_mul_f32_e32 v7, 0xbfb8aa3b, v7
	v_add_f32_e32 v5, 1.0, v5
	v_add_f32_e32 v6, 1.0, v6
	v_exp_f32_e32 v7, v7
	v_max_f32_e32 v9, v9, v9
	v_rcp_f32_e32 v5, v5
	v_rcp_f32_e32 v6, v6
	v_add_f32_e32 v2, 1.0, v2
	v_max_f32_e32 v9, 0xc1f00000, v9
	v_rcp_f32_e32 v2, v2
	v_mul_f32_e32 v9, 0xbfb8aa3b, v9
	v_exp_f32_e32 v9, v9
	v_add_f32_e32 v7, 1.0, v7
	v_mul_f32_e32 v5, v38, v5
	v_mul_f32_e32 v6, v39, v6
	v_rcp_f32_e32 v7, v7
	v_mul_f32_e32 v5, 0x41800000, v5
	v_mul_f32_e32 v6, 0x41800000, v6
	v_mul_f32_e32 v10, v41, v2
	v_mov_b32_e32 v2, v33
	v_cvt_pk_fp8_f32 v2, v5, v6
	v_add_f32_e32 v5, 1.0, v9
	v_cvt_f32_fp8_sdwa v9, v3 src0_sel:BYTE_1
	v_mul_f32_e32 v7, v40, v7
	v_mul_f32_e32 v7, 0x41800000, v7
	v_mul_f32_e32 v6, 0x41800000, v10
	v_cvt_pk_fp8_f32 v2, v7, v6 op_sel:[0,0,1]
	v_max_f32_e32 v6, v9, v9
	v_cvt_f32_fp8_sdwa v7, v3 src0_sel:BYTE_2
	v_cvt_f32_fp8_sdwa v3, v3 src0_sel:BYTE_3
	v_max_f32_e32 v6, 0xc1f00000, v6
	v_mul_f32_e32 v6, 0xbfb8aa3b, v6
	v_exp_f32_e32 v6, v6
	v_max_f32_e32 v7, v7, v7
	v_max_f32_e32 v7, 0xc1f00000, v7
	v_max_f32_e32 v3, 0xc1f00000, v3
	v_mul_f32_e32 v7, 0xbfb8aa3b, v7
	v_mul_f32_e32 v3, 0xbfb8aa3b, v3
	v_exp_f32_e32 v7, v7
	v_add_f32_e32 v6, 1.0, v6
	v_exp_f32_e32 v3, v3
	v_rcp_f32_e32 v5, v5
	v_rcp_f32_e32 v6, v6
	v_add_f32_e32 v7, 1.0, v7
	v_add_f32_e32 v3, 1.0, v3
	v_mul_f32_e32 v5, v34, v5
	v_rcp_f32_e32 v7, v7
	v_mul_f32_e32 v6, v35, v6
	v_rcp_f32_e32 v9, v3
	v_mul_f32_e32 v5, 0x41800000, v5
	v_mul_f32_e32 v6, 0x41800000, v6
	v_mov_b32_e32 v3, v33
	v_cvt_pk_fp8_f32 v3, v5, v6
	v_mul_f32_e32 v7, v36, v7
	v_mul_f32_e32 v6, v37, v9
	v_mul_f32_e32 v5, 0x41800000, v7
	v_mul_f32_e32 v6, 0x41800000, v6
	v_cvt_pk_fp8_f32 v3, v5, v6 op_sel:[0,0,1]
	global_store_dwordx4 v4, v[0:3], s[14:15]
	s_cbranch_vccnz .LBB0_803
	s_andn2_b64 vcc, exec, s[12:13]
	s_cbranch_vccnz .LBB0_802
	s_barrier
	s_branch .LBB0_802
